# speedup vs baseline: 1.0273x; 1.0038x over previous
.LBB0_2:
	s_or_b64 exec, exec, s[16:17]
	v_bfe_u32 v141, v0, 5, 1
	v_lshrrev_b32_e32 v4, 1, v0
	v_lshlrev_b32_e32 v72, 12, v141
	v_mov_b32_e32 v73, 0
	v_and_b32_e32 v142, 0x60, v4
	v_and_b32_e32 v76, 31, v0
	s_waitcnt lgkmcnt(0)
	v_lshl_add_u64 v[2:3], s[10:11], 0, v[72:73]
	v_lshlrev_b32_e32 v72, 2, v142
	v_lshl_add_u64 v[2:3], v[2:3], 0, v[72:73]
	v_lshlrev_b32_e32 v4, 2, v76
	v_mov_b32_e32 v5, v73
	v_lshl_add_u64 v[2:3], v[2:3], 0, v[4:5]
	s_movk_i32 s0, 0x2000
	v_add_co_u32_e32 v4, vcc, s0, v2
	v_and_b32_e32 v1, 0x78, v1
	s_nop 0
	v_addc_co_u32_e32 v5, vcc, 0, v3, vcc
	v_lshrrev_b32_e32 v40, 4, v0
	global_load_dword v140, v[2:3], off
	global_load_dword v136, v[2:3], off offset:512
	global_load_dword v137, v[2:3], off offset:1024
	global_load_dword v138, v[2:3], off offset:1536
	global_load_dword v139, v[2:3], off offset:2048
	global_load_dword v133, v[2:3], off offset:2560
	global_load_dword v134, v[2:3], off offset:3072
	global_load_dword v135, v[2:3], off offset:3584
	global_load_dword v120, v[4:5], off
	global_load_dword v121, v[4:5], off offset:512
	global_load_dword v122, v[4:5], off offset:1024
	global_load_dword v123, v[4:5], off offset:1536
	global_load_dword v124, v[4:5], off offset:2048
	global_load_dword v117, v[4:5], off offset:2560
	global_load_dword v118, v[4:5], off offset:3072
	global_load_dword v119, v[4:5], off offset:3584
	v_lshlrev_b32_e32 v4, 2, v1
	v_mov_b32_e32 v5, v73
	v_or_b32_e32 v74, s2, v40
	v_mov_b32_e32 v75, s3
	s_movk_i32 s0, 0x4000
	v_lshl_add_u64 v[4:5], s[4:5], 0, v[4:5]
	v_lshlrev_b64 v[8:9], 9, v[74:75]
	v_add_co_u32_e32 v6, vcc, s0, v2
	v_lshl_add_u64 v[8:9], v[4:5], 0, v[8:9]
	s_nop 0
	v_addc_co_u32_e32 v7, vcc, 0, v3, vcc
	global_load_dwordx4 v[10:13], v[8:9], off offset:16 nt
	global_load_dwordx4 v[14:17], v[8:9], off nt
	global_load_dword v132, v[6:7], off
	global_load_dword v128, v[6:7], off offset:512
	global_load_dword v129, v[6:7], off offset:1024
	global_load_dword v130, v[6:7], off offset:1536
	global_load_dword v131, v[6:7], off offset:2048
	global_load_dword v125, v[6:7], off offset:2560
	global_load_dword v126, v[6:7], off offset:3072
	global_load_dword v127, v[6:7], off offset:3584
	s_movk_i32 s0, 0x6000
	v_add_co_u32_e32 v6, vcc, s0, v2
	s_mov_b32 s0, 0x8000
	s_nop 0
	v_addc_co_u32_e32 v7, vcc, 0, v3, vcc
	global_load_dword v112, v[6:7], off
	global_load_dword v113, v[6:7], off offset:512
	global_load_dword v114, v[6:7], off offset:1024
	global_load_dword v115, v[6:7], off offset:1536
	global_load_dword v116, v[6:7], off offset:2048
	global_load_dword v109, v[6:7], off offset:2560
	global_load_dword v110, v[6:7], off offset:3072
	global_load_dword v111, v[6:7], off offset:3584
	v_add_co_u32_e32 v6, vcc, s0, v2
	s_mov_b32 s0, 0xa000
	s_nop 0
	v_addc_co_u32_e32 v7, vcc, 0, v3, vcc
	global_load_dword v108, v[6:7], off
	global_load_dword v104, v[6:7], off offset:512
	global_load_dword v105, v[6:7], off offset:1024
	global_load_dword v106, v[6:7], off offset:1536
	global_load_dword v107, v[6:7], off offset:2048
	global_load_dword v101, v[6:7], off offset:2560
	global_load_dword v102, v[6:7], off offset:3072
	global_load_dword v103, v[6:7], off offset:3584
	v_add_co_u32_e32 v6, vcc, s0, v2
	v_mov_b32_e32 v9, v73
	s_nop 0
	v_addc_co_u32_e32 v7, vcc, 0, v3, vcc
	global_load_dword v91, v[6:7], off
	global_load_dword v92, v[6:7], off offset:512
	global_load_dword v93, v[6:7], off offset:1024
	global_load_dword v94, v[6:7], off offset:1536
	global_load_dword v95, v[6:7], off offset:2048
	global_load_dword v88, v[6:7], off offset:2560
	global_load_dword v89, v[6:7], off offset:3072
	global_load_dword v90, v[6:7], off offset:3584
	v_or_b32_e32 v6, 0x100, v0
	v_lshrrev_b32_e32 v8, 4, v6
	v_lshl_add_u64 v[38:39], s[2:3], 0, v[8:9]
	v_lshlrev_b64 v[6:7], 9, v[38:39]
	v_lshl_add_u64 v[6:7], v[4:5], 0, v[6:7]
	global_load_dwordx4 v[18:21], v[6:7], off offset:16 nt
	global_load_dwordx4 v[22:25], v[6:7], off nt
	s_mov_b32 s0, 0xc000
	v_add_co_u32_e32 v6, vcc, s0, v2
	s_mov_b32 s0, 0xe000
	s_nop 0
	v_addc_co_u32_e32 v7, vcc, 0, v3, vcc
	v_add_co_u32_e32 v2, vcc, s0, v2
	global_load_dword v100, v[6:7], off
	global_load_dword v96, v[6:7], off offset:512
	global_load_dword v97, v[6:7], off offset:1024
	global_load_dword v98, v[6:7], off offset:1536
	global_load_dword v99, v[6:7], off offset:2048
	global_load_dword v85, v[6:7], off offset:2560
	global_load_dword v86, v[6:7], off offset:3072
	global_load_dword v87, v[6:7], off offset:3584
	v_addc_co_u32_e32 v3, vcc, 0, v3, vcc
	global_load_dword v80, v[2:3], off
	global_load_dword v81, v[2:3], off offset:512
	global_load_dword v82, v[2:3], off offset:1024
	global_load_dword v83, v[2:3], off offset:1536
	global_load_dword v84, v[2:3], off offset:2048
	global_load_dword v77, v[2:3], off offset:2560
	global_load_dword v78, v[2:3], off offset:3072
	global_load_dword v79, v[2:3], off offset:3584
	v_lshlrev_b32_e32 v2, 1, v1
	v_mov_b32_e32 v3, v73
	v_lshl_add_u64 v[6:7], s[14:15], 0, v[2:3]
	v_lshlrev_b64 v[30:31], 8, v[74:75]
	v_lshl_add_u64 v[30:31], v[6:7], 0, v[30:31]
	v_mov_b32_e32 v45, v73
	s_mov_b32 s0, 0x41800000
	s_mov_b32 s1, 0x3b800000
	s_movk_i32 s4, 0x110
	v_or_b32_e32 v3, 0x4400, v2
	s_waitcnt vmcnt(51)
	v_cvt_pk_f16_f32 v28, v10, v11
	s_waitcnt vmcnt(50)
	v_cvt_pk_f16_f32 v26, v14, v15
	v_cvt_pk_f16_f32 v27, v16, v17
	v_cvt_pk_f16_f32 v29, v12, v13
	global_store_dwordx4 v[30:31], v[26:29], off sc1
	v_mul_f32_e32 v1, 0x41800000, v14
	v_mul_f32_e32 v9, 0x41800000, v15
	v_or_b32_e32 v26, 0x200, v0
	v_lshrrev_b32_e32 v44, 4, v26
	v_lshl_add_u64 v[46:47], s[2:3], 0, v[44:45]
	v_lshlrev_b64 v[26:27], 9, v[46:47]
	v_lshl_add_u64 v[34:35], v[4:5], 0, v[26:27]
	global_load_dwordx4 v[26:29], v[34:35], off offset:16 nt
	global_load_dwordx4 v[30:33], v[34:35], off nt
	v_mul_f32_e32 v35, 0x41800000, v16
	v_mul_f32_e32 v36, 0x41800000, v17
	v_cvt_pk_f16_f32 v34, v1, v9
	v_mul_f32_e32 v37, 0x41800000, v10
	v_fma_mix_f32 v1, v14, s0, -v34 op_sel_hi:[0,0,1]
	v_mul_f32_e32 v41, 0x41800000, v11
	v_cvt_pk_f16_f32 v35, v35, v36
	v_cvt_pk_f16_f32 v36, v37, v41
	v_fma_mix_f32 v9, v15, s0, -v34 op_sel:[0,0,1] op_sel_hi:[0,0,1]
	v_fma_mix_f32 v14, v16, s0, -v35 op_sel_hi:[0,0,1]
	v_fma_mix_f32 v16, v10, s0, -v36 op_sel_hi:[0,0,1]
	v_cvt_pk_f16_f32 v10, v1, v9
	v_mad_u32_u24 v1, v40, s4, v2
	v_mul_f32_e32 v42, 0x41800000, v12
	v_mul_f32_e32 v43, 0x41800000, v13
	v_cvt_pk_f16_f32 v37, v42, v43
	ds_write_b128 v1, v[34:37]
	v_fma_mix_f32 v13, v13, s0, -v37 op_sel:[0,0,1] op_sel_hi:[0,0,1]
	v_mad_u32_u24 v1, v40, s4, v3
	v_or_b32_e32 v0, 0x300, v0
	v_fma_mix_f32 v15, v17, s0, -v35 op_sel:[0,0,1] op_sel_hi:[0,0,1]
	v_fma_mix_f32 v17, v11, s0, -v36 op_sel:[0,0,1] op_sel_hi:[0,0,1]
	v_fma_mix_f32 v41, v12, s0, -v37 op_sel_hi:[0,0,1]
	v_cvt_pk_f16_f32 v11, v14, v15
	v_cvt_pk_f16_f32 v12, v16, v17
	v_cvt_pk_f16_f32 v13, v41, v13
	ds_write_b128 v1, v[10:13]
	v_lshrrev_b32_e32 v0, 4, v0
	v_mov_b32_e32 v1, v73
	v_lshl_add_u64 v[48:49], s[2:3], 0, v[0:1]
	v_lshlrev_b64 v[10:11], 9, v[48:49]
	v_lshl_add_u64 v[4:5], v[4:5], 0, v[10:11]
	global_load_dwordx4 v[10:13], v[4:5], off offset:16 nt
	global_load_dwordx4 v[14:17], v[4:5], off nt
	v_lshlrev_b64 v[4:5], 8, v[38:39]
	s_waitcnt vmcnt(21)
	v_cvt_pk_f16_f32 v34, v22, v23
	v_lshl_add_u64 v[4:5], v[6:7], 0, v[4:5]
	v_mul_f32_e32 v1, 0x41800000, v22
	v_cvt_pk_f16_f32 v35, v24, v25
	v_cvt_pk_f16_f32 v36, v18, v19
	v_cvt_pk_f16_f32 v37, v20, v21
	global_store_dwordx4 v[4:5], v[34:37], off sc1
	v_mul_f32_e32 v4, 0x41800000, v23
	v_mul_f32_e32 v5, 0x41800000, v24
	v_cvt_pk_f16_f32 v34, v1, v4
	v_mul_f32_e32 v9, 0x41800000, v25
	v_fma_mix_f32 v1, v22, s0, -v34 op_sel_hi:[0,0,1]
	v_fma_mix_f32 v4, v23, s0, -v34 op_sel:[0,0,1] op_sel_hi:[0,0,1]
	v_cvt_pk_f16_f32 v22, v1, v4
	v_or_b32_e32 v1, v142, v76
	v_mul_f32_e32 v36, 0x41800000, v18
	v_cvt_pk_f16_f32 v35, v5, v9
	v_lshlrev_b32_e32 v4, 9, v1
	v_mov_b32_e32 v5, v73
	v_mul_f32_e32 v37, 0x41800000, v19
	v_mul_f32_e32 v38, 0x41800000, v20
	v_mul_f32_e32 v39, 0x41800000, v21
	v_cvt_pk_f16_f32 v36, v36, v37
	v_fma_mix_f32 v9, v24, s0, -v35 op_sel_hi:[0,0,1]
	v_fma_mix_f32 v23, v25, s0, -v35 op_sel:[0,0,1] op_sel_hi:[0,0,1]
	v_fma_mix_f32 v24, v18, s0, -v36 op_sel_hi:[0,0,1]
	v_fma_mix_f32 v25, v19, s0, -v36 op_sel:[0,0,1] op_sel_hi:[0,0,1]
	v_lshl_add_u64 v[4:5], s[6:7], 0, v[4:5]
	v_lshlrev_b32_e32 v18, 5, v141
	v_mov_b32_e32 v19, v73
	v_cvt_pk_f16_f32 v37, v38, v39
	v_mad_u32_u24 v1, v8, s4, v2
	v_fma_mix_f32 v38, v20, s0, -v37 op_sel_hi:[0,0,1]
	v_fma_mix_f32 v39, v21, s0, -v37 op_sel:[0,0,1] op_sel_hi:[0,0,1]
	v_lshl_add_u64 v[20:21], v[4:5], 0, v[18:19]
	global_load_dwordx4 v[64:67], v[20:21], off
	global_load_dwordx4 v[40:43], v[20:21], off offset:16
	v_lshlrev_b64 v[4:5], 8, v[46:47]
	v_cvt_pk_f16_f32 v23, v9, v23
	v_cvt_pk_f16_f32 v24, v24, v25
	v_cvt_pk_f16_f32 v25, v38, v39
	ds_write_b128 v1, v[34:37]
	v_mad_u32_u24 v1, v8, s4, v3
	v_lshl_add_u64 v[4:5], v[6:7], 0, v[4:5]
	ds_write_b128 v1, v[22:25]
	s_waitcnt vmcnt(5)
	v_cvt_pk_f16_f32 v22, v30, v31
	v_cvt_pk_f16_f32 v23, v32, v33
	v_cvt_pk_f16_f32 v24, v26, v27
	v_cvt_pk_f16_f32 v25, v28, v29
	global_store_dwordx4 v[4:5], v[22:25], off sc1
	v_mul_f32_e32 v4, 0x41800000, v31
	v_mul_f32_e32 v5, 0x41800000, v32
	v_mul_f32_e32 v1, 0x41800000, v30
	v_mul_f32_e32 v8, 0x41800000, v33
	v_mul_f32_e32 v9, 0x41800000, v26
	v_mul_f32_e32 v18, 0x41800000, v27
	v_cvt_pk_f16_f32 v22, v1, v4
	v_cvt_pk_f16_f32 v23, v5, v8
	global_load_dwordx4 v[52:55], v[20:21], off offset:64
	v_fma_mix_f32 v4, v31, s0, -v22 op_sel:[0,0,1] op_sel_hi:[0,0,1]
	v_fma_mix_f32 v5, v32, s0, -v23 op_sel_hi:[0,0,1]
	v_cvt_pk_f16_f32 v24, v9, v18
	v_fma_mix_f32 v1, v30, s0, -v22 op_sel_hi:[0,0,1]
	v_fma_mix_f32 v8, v33, s0, -v23 op_sel:[0,0,1] op_sel_hi:[0,0,1]
	v_fma_mix_f32 v9, v26, s0, -v24 op_sel_hi:[0,0,1]
	v_fma_mix_f32 v18, v27, s0, -v24 op_sel:[0,0,1] op_sel_hi:[0,0,1]
	v_cvt_pk_f16_f32 v26, v1, v4
	v_cvt_pk_f16_f32 v27, v5, v8
	v_lshlrev_b64 v[4:5], 8, v[48:49]
	global_load_dwordx4 v[48:51], v[20:21], off offset:80
	v_mul_f32_e32 v25, 0x41800000, v29
	v_mad_u32_u24 v1, v44, s4, v2
	v_mul_f32_e32 v19, 0x41800000, v28
	v_cvt_pk_f16_f32 v25, v19, v25
	ds_write_b128 v1, v[22:25]
	v_fma_mix_f32 v29, v29, s0, -v25 op_sel:[0,0,1] op_sel_hi:[0,0,1]
	v_mad_u32_u24 v1, v44, s4, v3
	v_lshl_add_u64 v[4:5], v[6:7], 0, v[4:5]
	v_fma_mix_f32 v19, v28, s0, -v25 op_sel_hi:[0,0,1]
	v_cvt_pk_f16_f32 v28, v9, v18
	v_cvt_pk_f16_f32 v29, v19, v29
	ds_write_b128 v1, v[26:29]
	s_waitcnt vmcnt(6)
	v_cvt_pk_f16_f32 v22, v14, v15
	v_cvt_pk_f16_f32 v23, v16, v17
	v_cvt_pk_f16_f32 v24, v10, v11
	v_cvt_pk_f16_f32 v25, v12, v13
	global_store_dwordx4 v[4:5], v[22:25], off sc1
	v_mul_f32_e32 v1, 0x41800000, v14
	v_mul_f32_e32 v4, 0x41800000, v15
	v_mul_f32_e32 v5, 0x41800000, v16
	v_mul_f32_e32 v6, 0x41800000, v17
	v_mul_f32_e32 v8, 0x41800000, v11
	v_mul_f32_e32 v7, 0x41800000, v10
	v_mul_f32_e32 v9, 0x41800000, v12
	v_cvt_pk_f16_f32 v4, v1, v4
	v_cvt_pk_f16_f32 v5, v5, v6
	v_cvt_pk_f16_f32 v6, v7, v8
	v_mul_f32_e32 v18, 0x41800000, v13
	v_fma_mix_f32 v1, v14, s0, -v4 op_sel_hi:[0,0,1]
	v_fma_mix_f32 v8, v15, s0, -v4 op_sel:[0,0,1] op_sel_hi:[0,0,1]
	v_cvt_pk_f16_f32 v7, v9, v18
	v_fma_mix_f32 v9, v16, s0, -v5 op_sel_hi:[0,0,1]
	v_fma_mix_f32 v10, v10, s0, -v6 op_sel_hi:[0,0,1]
	v_fma_mix_f32 v11, v11, s0, -v6 op_sel:[0,0,1] op_sel_hi:[0,0,1]
	v_cvt_pk_f16_f32 v8, v1, v8
	v_mad_u32_u24 v1, v0, s4, v2
	v_mad_u32_u24 v0, v0, s4, v3
	v_fma_mix_f32 v14, v17, s0, -v5 op_sel:[0,0,1] op_sel_hi:[0,0,1]
	v_fma_mix_f32 v12, v12, s0, -v7 op_sel_hi:[0,0,1]
	v_fma_mix_f32 v13, v13, s0, -v7 op_sel:[0,0,1] op_sel_hi:[0,0,1]
	v_cvt_pk_f16_f32 v9, v9, v14
	v_cvt_pk_f16_f32 v10, v10, v11
	v_cvt_pk_f16_f32 v11, v12, v13
	ds_write_b128 v1, v[4:7]
	ds_write_b128 v0, v[8:11]
	s_waitcnt vmcnt(5)
	v_mul_f32_e32 v0, 0x43800000, v64
	v_mul_f32_e32 v1, 0x43800000, v65
	v_mul_f32_e32 v2, 0x43800000, v66
	v_mul_f32_e32 v3, 0x43800000, v67
	s_waitcnt vmcnt(4)
	v_mul_f32_e32 v4, 0x43800000, v40
	v_mul_f32_e32 v5, 0x43800000, v41
	v_mul_f32_e32 v6, 0x43800000, v42
	v_mul_f32_e32 v7, 0x43800000, v43
	v_cvt_pk_f16_f32 v60, v0, v1
	v_cvt_pk_f16_f32 v61, v2, v3
	v_cvt_pk_f16_f32 v62, v4, v5
	v_cvt_pk_f16_f32 v63, v6, v7
	v_cmp_gt_u32_e32 vcc, 8, v187
	s_nop 1
	s_and_saveexec_b64 s[16:17], vcc
	s_cbranch_execz .Lmy_wg_skip
	v_cvt_pk_f16_f32 v176, v176, v177
	v_cvt_pk_f16_f32 v177, v178, v179
	v_cvt_pk_f16_f32 v178, v180, v181
	v_cvt_pk_f16_f32 v179, v182, v183
	global_store_dwordx4 v[184:185], v[176:179], off
.Lmy_wg_skip:
	s_or_b64 exec, exec, s[16:17]
	global_load_dwordx4 v[44:47], v[20:21], off offset:144
	global_load_dwordx4 v[56:59], v[20:21], off offset:128
	global_load_dwordx4 v[0:3], v[20:21], off offset:208
	global_load_dwordx4 v[8:11], v[20:21], off offset:192
	global_load_dwordx4 v[4:7], v[20:21], off offset:272
	global_load_dwordx4 v[12:15], v[20:21], off offset:256
	v_lshl_add_u64 v[16:17], s[8:9], 0, v[72:73]
	v_lshlrev_b32_e32 v72, 4, v141
	v_lshl_add_u64 v[16:17], v[16:17], 0, v[72:73]
	v_mad_u32_u24 v74, v76, s4, v72
	global_load_dwordx4 v[156:159], v[16:17], off
	global_load_dwordx4 v[152:155], v[16:17], off offset:32
	global_load_dwordx4 v[148:151], v[16:17], off offset:64
	global_load_dwordx4 v[144:147], v[16:17], off offset:96
	global_load_dwordx4 v[32:35], v[20:21], off offset:336
	global_load_dwordx4 v[36:39], v[20:21], off offset:320
	global_load_dwordx4 v[24:27], v[20:21], off offset:400
	global_load_dwordx4 v[28:31], v[20:21], off offset:384
	s_nop 0
	global_load_dwordx4 v[16:19], v[20:21], off offset:464
	s_nop 0
	global_load_dwordx4 v[20:23], v[20:21], off offset:448
	s_waitcnt lgkmcnt(0)
	s_barrier
	ds_read_b128 v[68:71], v74
	s_mov_b32 s3, 0x43800000
	v_fma_mix_f32 v143, v64, s3, -v60 op_sel_hi:[0,0,1]
	v_fma_mix_f32 v160, v65, s3, -v60 op_sel:[0,0,1] op_sel_hi:[0,0,1]
	v_fma_mix_f32 v161, v66, s3, -v61 op_sel_hi:[0,0,1]
	v_fma_mix_f32 v162, v67, s3, -v61 op_sel:[0,0,1] op_sel_hi:[0,0,1]
	ds_read_b128 v[64:67], v74 offset:32
	s_waitcnt lgkmcnt(1)
	v_mfma_f32_32x32x16_f16 a[16:31], v[60:63], v[68:71], 0
	v_fma_mix_f32 v163, v40, s3, -v62 op_sel_hi:[0,0,1]
	v_fma_mix_f32 v43, v43, s3, -v63 op_sel:[0,0,1] op_sel_hi:[0,0,1]
	v_fma_mix_f32 v164, v41, s3, -v62 op_sel:[0,0,1] op_sel_hi:[0,0,1]
	v_fma_mix_f32 v165, v42, s3, -v63 op_sel_hi:[0,0,1]
	v_cvt_pk_f16_f32 v40, v143, v160
	v_cvt_pk_f16_f32 v41, v161, v162
	v_cvt_pk_f16_f32 v42, v163, v164
	v_cvt_pk_f16_f32 v43, v165, v43
	s_nop 0
	v_mfma_f32_32x32x16_f16 a[16:31], v[40:43], v[68:71], a[16:31]
	ds_read_b128 v[68:71], v74 offset:8704
	ds_read_b128 v[160:163], v74 offset:8736
	s_waitcnt lgkmcnt(1)
	v_mfma_f32_32x32x16_f16 a[0:15], v[60:63], v[68:71], 0
	v_mfma_f32_32x32x16_f16 a[0:15], v[40:43], v[68:71], a[0:15]
	v_mov_b32_e32 v40, 0x4400
	v_mad_u32_u24 v41, v76, s4, v40
	v_add_u32_e32 v40, v41, v72
	ds_read_b128 v[68:71], v40
	ds_read_b128 v[164:167], v40 offset:32
	s_waitcnt vmcnt(18)
	v_mul_f32_e32 v42, 0x43800000, v52
	v_mul_f32_e32 v43, 0x43800000, v53
	s_waitcnt lgkmcnt(1)
	v_mfma_f32_32x32x16_f16 a[16:31], v[60:63], v[68:71], a[16:31]
	ds_read_b128 v[68:71], v40 offset:8704
	ds_read_b128 v[168:171], v40 offset:8736
	s_waitcnt lgkmcnt(1)
	v_mfma_f32_32x32x16_f16 a[0:15], v[60:63], v[68:71], a[0:15]
	v_mul_f32_e32 v61, 0x43800000, v54
	v_mul_f32_e32 v62, 0x43800000, v55
	v_cvt_pk_f16_f32 v60, v42, v43
	v_cvt_pk_f16_f32 v61, v61, v62
	s_nop 0
	v_fma_mix_f32 v42, v52, s3, -v60 op_sel_hi:[0,0,1]
	v_fma_mix_f32 v43, v53, s3, -v60 op_sel:[0,0,1] op_sel_hi:[0,0,1]
	v_fma_mix_f32 v52, v54, s3, -v61 op_sel_hi:[0,0,1]
	v_fma_mix_f32 v53, v55, s3, -v61 op_sel:[0,0,1] op_sel_hi:[0,0,1]
	s_waitcnt vmcnt(17)
	v_mul_f32_e32 v54, 0x43800000, v48
	v_mul_f32_e32 v55, 0x43800000, v49
	v_cvt_pk_f16_f32 v62, v54, v55
	v_mul_f32_e32 v54, 0x43800000, v50
	v_mul_f32_e32 v55, 0x43800000, v51
	v_cvt_pk_f16_f32 v63, v54, v55
	v_fma_mix_f32 v54, v48, s3, -v62 op_sel_hi:[0,0,1]
	v_mfma_f32_32x32x16_f16 a[16:31], v[60:63], v[64:67], a[16:31]
	v_fma_mix_f32 v51, v51, s3, -v63 op_sel:[0,0,1] op_sel_hi:[0,0,1]
	v_fma_mix_f32 v55, v49, s3, -v62 op_sel:[0,0,1] op_sel_hi:[0,0,1]
	v_fma_mix_f32 v68, v50, s3, -v63 op_sel_hi:[0,0,1]
	v_cvt_pk_f16_f32 v48, v42, v43
	v_cvt_pk_f16_f32 v49, v52, v53
	v_cvt_pk_f16_f32 v50, v54, v55
	v_cvt_pk_f16_f32 v51, v68, v51
	v_mfma_f32_32x32x16_f16 a[0:15], v[60:63], v[160:163], a[0:15]
	ds_read_b128 v[52:55], v74 offset:64
	s_waitcnt vmcnt(14)
	v_mul_f32_e32 v42, 0x43800000, v56
	v_mul_f32_e32 v43, 0x43800000, v57
	v_mfma_f32_32x32x16_f16 a[16:31], v[48:51], v[64:67], a[16:31]
	v_mfma_f32_32x32x16_f16 a[0:15], v[48:51], v[160:163], a[0:15]
	v_mul_f32_e32 v49, 0x43800000, v58
	v_mul_f32_e32 v50, 0x43800000, v59
	v_cvt_pk_f16_f32 v49, v49, v50
	v_mul_f32_e32 v50, 0x43800000, v44
	v_mul_f32_e32 v51, 0x43800000, v45
	v_cvt_pk_f16_f32 v48, v42, v43
	v_cvt_pk_f16_f32 v50, v50, v51
	v_mfma_f32_32x32x16_f16 a[16:31], v[60:63], v[164:167], a[16:31]
	v_fma_mix_f32 v42, v56, s3, -v48 op_sel_hi:[0,0,1]
	v_mul_f32_e32 v51, 0x43800000, v46
	v_mul_f32_e32 v56, 0x43800000, v47
	v_fma_mix_f32 v43, v57, s3, -v48 op_sel:[0,0,1] op_sel_hi:[0,0,1]
	v_cvt_pk_f16_f32 v51, v51, v56
	v_fma_mix_f32 v44, v44, s3, -v50 op_sel_hi:[0,0,1]
	v_fma_mix_f32 v45, v45, s3, -v50 op_sel:[0,0,1] op_sel_hi:[0,0,1]
	s_waitcnt lgkmcnt(1)
	v_mfma_f32_32x32x16_f16 a[0:15], v[60:63], v[168:171], a[0:15]
	v_fma_mix_f32 v60, v58, s3, -v49 op_sel_hi:[0,0,1]
	v_fma_mix_f32 v61, v59, s3, -v49 op_sel:[0,0,1] op_sel_hi:[0,0,1]
	ds_read_b128 v[56:59], v74 offset:96
	v_fma_mix_f32 v46, v46, s3, -v51 op_sel_hi:[0,0,1]
	v_fma_mix_f32 v47, v47, s3, -v51 op_sel:[0,0,1] op_sel_hi:[0,0,1]
	v_cvt_pk_f16_f32 v42, v42, v43
	v_cvt_pk_f16_f32 v43, v60, v61
	s_waitcnt lgkmcnt(1)
	v_mfma_f32_32x32x16_f16 a[16:31], v[48:51], v[52:55], a[16:31]
	v_cvt_pk_f16_f32 v44, v44, v45
	v_cvt_pk_f16_f32 v45, v46, v47
	s_waitcnt vmcnt(13)
	v_mul_f32_e32 v46, 0x43800000, v3
	v_mfma_f32_32x32x16_f16 a[16:31], v[42:45], v[52:55], a[16:31]
	ds_read_b128 v[52:55], v74 offset:8768
	ds_read_b128 v[60:63], v74 offset:8800
	s_waitcnt lgkmcnt(1)
	v_mfma_f32_32x32x16_f16 a[0:15], v[48:51], v[52:55], a[0:15]
	v_mfma_f32_32x32x16_f16 a[0:15], v[42:45], v[52:55], a[0:15]
	ds_read_b128 v[42:45], v40 offset:64
	ds_read_b128 v[52:55], v40 offset:96
	s_waitcnt lgkmcnt(1)
	v_mfma_f32_32x32x16_f16 a[16:31], v[48:51], v[42:45], a[16:31]
	ds_read_b128 v[42:45], v40 offset:8768
	ds_read_b128 v[64:67], v40 offset:8800
	s_waitcnt lgkmcnt(1)
	v_mfma_f32_32x32x16_f16 a[0:15], v[48:51], v[42:45], a[0:15]
	s_waitcnt vmcnt(12)
	v_mul_f32_e32 v42, 0x43800000, v8
	v_mul_f32_e32 v43, 0x43800000, v9
	v_mul_f32_e32 v44, 0x43800000, v10
	v_mul_f32_e32 v45, 0x43800000, v11
	v_cvt_pk_f16_f32 v42, v42, v43
	v_cvt_pk_f16_f32 v43, v44, v45
	v_mul_f32_e32 v44, 0x43800000, v0
	v_mul_f32_e32 v45, 0x43800000, v1
	v_cvt_pk_f16_f32 v44, v44, v45
	v_mul_f32_e32 v45, 0x43800000, v2
	v_cvt_pk_f16_f32 v45, v45, v46
	v_fma_mix_f32 v8, v8, s3, -v42 op_sel_hi:[0,0,1]
	v_fma_mix_f32 v3, v3, s3, -v45 op_sel:[0,0,1] op_sel_hi:[0,0,1]
	v_mfma_f32_32x32x16_f16 a[16:31], v[42:45], v[56:59], a[16:31]
	v_fma_mix_f32 v9, v9, s3, -v42 op_sel:[0,0,1] op_sel_hi:[0,0,1]
	v_fma_mix_f32 v10, v10, s3, -v43 op_sel_hi:[0,0,1]
	v_fma_mix_f32 v11, v11, s3, -v43 op_sel:[0,0,1] op_sel_hi:[0,0,1]
	v_fma_mix_f32 v46, v0, s3, -v44 op_sel_hi:[0,0,1]
	v_fma_mix_f32 v47, v1, s3, -v44 op_sel:[0,0,1] op_sel_hi:[0,0,1]
	v_fma_mix_f32 v48, v2, s3, -v45 op_sel_hi:[0,0,1]
	v_cvt_pk_f16_f32 v0, v8, v9
	v_cvt_pk_f16_f32 v1, v10, v11
	v_cvt_pk_f16_f32 v2, v46, v47
	v_cvt_pk_f16_f32 v3, v48, v3
	s_waitcnt vmcnt(10)
	v_mul_f32_e32 v8, 0x43800000, v12
	v_mfma_f32_32x32x16_f16 a[16:31], v[0:3], v[56:59], a[16:31]
	v_mul_f32_e32 v9, 0x43800000, v13
	v_mul_f32_e32 v10, 0x43800000, v14
	v_mul_f32_e32 v11, 0x43800000, v15
	v_cvt_pk_f16_f32 v8, v8, v9
	v_cvt_pk_f16_f32 v9, v10, v11
	v_mul_f32_e32 v10, 0x43800000, v4
	v_fma_mix_f32 v50, v12, s3, -v8 op_sel_hi:[0,0,1]
	v_mfma_f32_32x32x16_f16 a[16:31], v[42:45], v[52:55], a[16:31]
	v_fma_mix_f32 v51, v13, s3, -v8 op_sel:[0,0,1] op_sel_hi:[0,0,1]
	v_fma_mix_f32 v52, v14, s3, -v9 op_sel_hi:[0,0,1]
	v_fma_mix_f32 v53, v15, s3, -v9 op_sel:[0,0,1] op_sel_hi:[0,0,1]
	ds_read_b128 v[12:15], v74 offset:128
	v_mul_f32_e32 v11, 0x43800000, v5
	v_cvt_pk_f16_f32 v10, v10, v11
	v_mul_f32_e32 v11, 0x43800000, v6
	v_mul_f32_e32 v46, 0x43800000, v7
	v_cvt_pk_f16_f32 v11, v11, v46
	ds_read_b128 v[46:49], v74 offset:160
	s_waitcnt lgkmcnt(1)
	v_mfma_f32_32x32x16_f16 a[16:31], v[8:11], v[12:15], a[16:31]
	v_fma_mix_f32 v7, v7, s3, -v11 op_sel:[0,0,1] op_sel_hi:[0,0,1]
	v_fma_mix_f32 v54, v4, s3, -v10 op_sel_hi:[0,0,1]
	v_fma_mix_f32 v55, v5, s3, -v10 op_sel:[0,0,1] op_sel_hi:[0,0,1]
	v_fma_mix_f32 v56, v6, s3, -v11 op_sel_hi:[0,0,1]
	v_cvt_pk_f16_f32 v4, v50, v51
	v_cvt_pk_f16_f32 v5, v52, v53
	v_cvt_pk_f16_f32 v6, v54, v55
	v_cvt_pk_f16_f32 v7, v56, v7
	s_waitcnt vmcnt(5)
	v_mul_f32_e32 v54, 0x43800000, v35
	v_mfma_f32_32x32x16_f16 a[16:31], v[4:7], v[12:15], a[16:31]
	ds_read_b128 v[12:15], v40 offset:128
	ds_read_b128 v[50:53], v40 offset:160
	v_mul_f32_e32 v57, 0x43800000, v135
	s_waitcnt lgkmcnt(1)
	v_mfma_f32_32x32x16_f16 a[16:31], v[8:11], v[12:15], a[16:31]
	s_waitcnt vmcnt(4)
	v_mul_f32_e32 v12, 0x43800000, v36
	v_mul_f32_e32 v13, 0x43800000, v37
	v_mul_f32_e32 v14, 0x43800000, v38
	v_mul_f32_e32 v15, 0x43800000, v39
	v_cvt_pk_f16_f32 v12, v12, v13
	v_cvt_pk_f16_f32 v13, v14, v15
	v_mul_f32_e32 v14, 0x43800000, v32
	v_mul_f32_e32 v15, 0x43800000, v33
	v_cvt_pk_f16_f32 v14, v14, v15
	v_mul_f32_e32 v15, 0x43800000, v34
	v_cvt_pk_f16_f32 v15, v15, v54
	v_fma_mix_f32 v36, v36, s3, -v12 op_sel_hi:[0,0,1]
	v_fma_mix_f32 v35, v35, s3, -v15 op_sel:[0,0,1] op_sel_hi:[0,0,1]
	v_mfma_f32_32x32x16_f16 a[16:31], v[12:15], v[46:49], a[16:31]
	v_fma_mix_f32 v37, v37, s3, -v12 op_sel:[0,0,1] op_sel_hi:[0,0,1]
	v_fma_mix_f32 v38, v38, s3, -v13 op_sel_hi:[0,0,1]
	v_fma_mix_f32 v39, v39, s3, -v13 op_sel:[0,0,1] op_sel_hi:[0,0,1]
	v_fma_mix_f32 v54, v32, s3, -v14 op_sel_hi:[0,0,1]
	v_fma_mix_f32 v55, v33, s3, -v14 op_sel:[0,0,1] op_sel_hi:[0,0,1]
	v_fma_mix_f32 v56, v34, s3, -v15 op_sel_hi:[0,0,1]
	v_cvt_pk_f16_f32 v32, v36, v37
	v_cvt_pk_f16_f32 v33, v38, v39
	v_cvt_pk_f16_f32 v34, v54, v55
	v_cvt_pk_f16_f32 v35, v56, v35
	s_waitcnt vmcnt(2)
	v_mul_f32_e32 v36, 0x43800000, v28
	v_mfma_f32_32x32x16_f16 a[16:31], v[32:35], v[46:49], a[16:31]
	v_mul_f32_e32 v37, 0x43800000, v29
	v_mul_f32_e32 v38, 0x43800000, v30
	v_mul_f32_e32 v39, 0x43800000, v31
	v_cvt_pk_f16_f32 v36, v36, v37
	v_cvt_pk_f16_f32 v37, v38, v39
	v_mul_f32_e32 v38, 0x43800000, v24
	v_mul_f32_e32 v39, 0x43800000, v25
	s_waitcnt lgkmcnt(0)
	v_mfma_f32_32x32x16_f16 a[16:31], v[12:15], v[50:53], a[16:31]
	v_fma_mix_f32 v50, v28, s3, -v36 op_sel_hi:[0,0,1]
	v_fma_mix_f32 v51, v29, s3, -v36 op_sel:[0,0,1] op_sel_hi:[0,0,1]
	v_fma_mix_f32 v52, v30, s3, -v37 op_sel_hi:[0,0,1]
	v_fma_mix_f32 v53, v31, s3, -v37 op_sel:[0,0,1] op_sel_hi:[0,0,1]
	ds_read_b128 v[28:31], v74 offset:192
	v_cvt_pk_f16_f32 v38, v38, v39
	v_mul_f32_e32 v39, 0x43800000, v26
	v_mul_f32_e32 v46, 0x43800000, v27
	v_mfma_f32_32x32x16_f16 a[0:15], v[42:45], v[60:63], a[0:15]
	v_cvt_pk_f16_f32 v39, v39, v46
	ds_read_b128 v[46:49], v74 offset:224
	v_fma_mix_f32 v27, v27, s3, -v39 op_sel:[0,0,1] op_sel_hi:[0,0,1]
	v_fma_mix_f32 v54, v24, s3, -v38 op_sel_hi:[0,0,1]
	v_fma_mix_f32 v55, v25, s3, -v38 op_sel:[0,0,1] op_sel_hi:[0,0,1]
	v_fma_mix_f32 v56, v26, s3, -v39 op_sel_hi:[0,0,1]
	v_cvt_pk_f16_f32 v24, v50, v51
	s_waitcnt lgkmcnt(1)
	v_mfma_f32_32x32x16_f16 a[16:31], v[36:39], v[28:31], a[16:31]
	v_cvt_pk_f16_f32 v25, v52, v53
	v_cvt_pk_f16_f32 v26, v54, v55
	v_cvt_pk_f16_f32 v27, v56, v27
	s_waitcnt vmcnt(1)
	v_mul_f32_e32 v54, 0x43800000, v19
	v_mfma_f32_32x32x16_f16 a[0:15], v[0:3], v[60:63], a[0:15]
	v_mfma_f32_32x32x16_f16 a[16:31], v[24:27], v[28:31], a[16:31]
	ds_read_b128 v[28:31], v40 offset:192
	ds_read_b128 v[50:53], v40 offset:224
	v_mfma_f32_32x32x16_f16 a[0:15], v[42:45], v[64:67], a[0:15]
	v_mov_b32_e32 v44, v158
	v_mov_b32_e32 v42, v159
	s_waitcnt lgkmcnt(1)
	v_mfma_f32_32x32x16_f16 a[16:31], v[36:39], v[28:31], a[16:31]
	s_waitcnt vmcnt(0)
	v_mul_f32_e32 v28, 0x43800000, v20
	v_mul_f32_e32 v29, 0x43800000, v21
	v_mul_f32_e32 v30, 0x43800000, v22
	v_mul_f32_e32 v31, 0x43800000, v23
	v_cvt_pk_f16_f32 v28, v28, v29
	v_cvt_pk_f16_f32 v29, v30, v31
	v_mul_f32_e32 v30, 0x43800000, v16
	v_mul_f32_e32 v31, 0x43800000, v17
	v_fma_mix_f32 v20, v20, s3, -v28 op_sel_hi:[0,0,1]
	v_fma_mix_f32 v21, v21, s3, -v28 op_sel:[0,0,1] op_sel_hi:[0,0,1]
	v_fma_mix_f32 v22, v22, s3, -v29 op_sel_hi:[0,0,1]
	v_fma_mix_f32 v23, v23, s3, -v29 op_sel:[0,0,1] op_sel_hi:[0,0,1]
	v_cvt_pk_f16_f32 v30, v30, v31
	v_mul_f32_e32 v31, 0x43800000, v18
	v_cvt_pk_f16_f32 v31, v31, v54
	v_fma_mix_f32 v54, v16, s3, -v30 op_sel_hi:[0,0,1]
	v_fma_mix_f32 v55, v17, s3, -v30 op_sel:[0,0,1] op_sel_hi:[0,0,1]
	v_cvt_pk_f16_f32 v16, v20, v21
	v_cvt_pk_f16_f32 v17, v22, v23
	ds_read_b128 v[0:3], v74 offset:8832
	ds_read_b128 v[20:23], v74 offset:8864
	s_waitcnt lgkmcnt(1)
	v_mfma_f32_32x32x16_f16 a[0:15], v[8:11], v[0:3], a[0:15]
	v_fma_mix_f32 v19, v19, s3, -v31 op_sel:[0,0,1] op_sel_hi:[0,0,1]
	v_fma_mix_f32 v56, v18, s3, -v31 op_sel_hi:[0,0,1]
	v_cvt_pk_f16_f32 v18, v54, v55
	v_cvt_pk_f16_f32 v19, v56, v19
	v_mul_f32_e32 v54, 0x43800000, v139
	v_mul_f32_e32 v55, 0x43800000, v133
	v_mul_f32_e32 v56, 0x43800000, v134
	v_mfma_f32_32x32x16_f16 a[0:15], v[4:7], v[0:3], a[0:15]
	ds_read_b128 v[0:3], v40 offset:8832
	ds_read_b128 v[4:7], v40 offset:8864
	s_waitcnt lgkmcnt(1)
	v_mfma_f32_32x32x16_f16 a[0:15], v[8:11], v[0:3], a[0:15]
	ds_read_b128 v[0:3], v74 offset:8896
	ds_read_b128 v[8:11], v74 offset:8928
	v_mfma_f32_32x32x16_f16 a[0:15], v[12:15], v[20:23], a[0:15]
	v_mfma_f32_32x32x16_f16 a[0:15], v[32:35], v[20:23], a[0:15]
	v_mov_b32_e32 v32, v155
	v_mov_b32_e32 v34, v154
	s_waitcnt lgkmcnt(2)
	v_mfma_f32_32x32x16_f16 a[0:15], v[12:15], v[4:7], a[0:15]
	ds_read_b128 v[12:15], v40 offset:8896
	ds_read_b128 v[20:23], v40 offset:8928
	s_waitcnt lgkmcnt(0)
	s_barrier
	v_mfma_f32_32x32x16_f16 a[0:15], v[36:39], v[0:3], a[0:15]
	v_mfma_f32_32x32x16_f16 a[0:15], v[24:27], v[0:3], a[0:15]
	v_mov_b32_e32 v26, v148
	v_mov_b32_e32 v24, v149
	v_mfma_f32_32x32x16_f16 a[0:15], v[36:39], v[12:15], a[0:15]
	v_mov_b32_e32 v38, v152
	v_mov_b32_e32 v36, v153
	v_mfma_f32_32x32x16_f16 a[16:31], v[28:31], v[46:49], a[16:31]
	v_mfma_f32_32x32x16_f16 a[0:15], v[28:31], v[8:11], a[0:15]
	v_mfma_f32_32x32x16_f16 a[16:31], v[16:19], v[46:49], a[16:31]
	v_mov_b32_e32 v48, v156
	v_mov_b32_e32 v46, v157
	v_mfma_f32_32x32x16_f16 a[0:15], v[16:19], v[8:11], a[0:15]
	v_mfma_f32_32x32x16_f16 a[16:31], v[28:31], v[50:53], a[16:31]
	v_mul_f32_e32 v50, 0x43800000, v140
	v_mul_f32_e32 v51, 0x43800000, v136
	v_mul_f32_e32 v52, 0x43800000, v137
	v_mul_f32_e32 v53, 0x43800000, v138
	v_mfma_f32_32x32x16_f16 a[0:15], v[28:31], v[20:23], a[0:15]
	s_nop 6
	v_accvgpr_read_b32 v45, a18
	v_accvgpr_read_b32 v47, a17
	v_accvgpr_read_b32 v49, a16
	v_mul_f32_e64 v8, v48, s0
	v_mul_f32_e64 v9, v49, s1
	v_pk_mul_f32 v[10:11], v[46:47], s[0:1]
	v_pk_mul_f32 v[16:17], v[44:45], s[0:1]
	v_add_f32_e32 v0, v8, v9
	v_accvgpr_read_b32 v43, a19
	v_accvgpr_read_b32 v2, a0
	v_accvgpr_read_b32 v4, a1
	v_accvgpr_read_b32 v6, a2
	v_fmac_f32_e32 v8, 0x3b800000, v2
	v_add_f32_e32 v2, v10, v11
	v_fmac_f32_e32 v10, 0x3b800000, v4
	v_add_f32_e32 v4, v16, v17
	v_fmac_f32_e32 v16, 0x3b800000, v6
	v_cvt_pk_f16_f32 v20, v0, v2
	v_pk_mul_f32 v[18:19], v[42:43], s[0:1]
	v_cvt_f32_f16_e32 v6, v20
	v_cvt_f32_f16_sdwa v9, v20 dst_sel:DWORD dst_unused:UNUSED_PAD src0_sel:WORD_1
	v_add_f32_e32 v11, v18, v19
	v_cvt_pk_f16_f32 v21, v4, v11
	v_sub_f32_e32 v0, v0, v6
	v_cvt_f32_f16_e32 v6, v21
	v_sub_f32_e32 v2, v2, v9
	v_cvt_f32_f16_sdwa v9, v21 dst_sel:DWORD dst_unused:UNUSED_PAD src0_sel:WORD_1
	v_cvt_pk_f16_f32 v22, v0, v2
	v_accvgpr_read_b32 v2, a3
	v_sub_f32_e32 v4, v4, v6
	v_cvt_pk_f16_f32 v28, v8, v10
	v_fmac_f32_e32 v18, 0x3b800000, v2
	v_cvt_f32_f16_e32 v0, v28
	v_cvt_f32_f16_sdwa v2, v28 dst_sel:DWORD dst_unused:UNUSED_PAD src0_sel:WORD_1
	v_sub_f32_e32 v6, v11, v9
	v_cvt_pk_f16_f32 v23, v4, v6
	v_cvt_pk_f16_f32 v29, v16, v18
	v_accvgpr_read_b32 v37, a21
	v_cvt_f32_f16_e32 v4, v29
	v_accvgpr_read_b32 v39, a20
	v_sub_f32_e32 v0, v8, v0
	v_cvt_f32_f16_sdwa v6, v29 dst_sel:DWORD dst_unused:UNUSED_PAD src0_sel:WORD_1
	v_sub_f32_e32 v2, v10, v2
	v_accvgpr_read_b32 v33, a23
	v_sub_f32_e32 v4, v16, v4
	v_cvt_pk_f16_f32 v8, v0, v2
	v_lshlrev_b32_e32 v0, 1, v142
	v_pk_mul_f32 v[10:11], v[38:39], s[0:1]
	v_accvgpr_read_b32 v2, a4
	v_pk_mul_f32 v[16:17], v[36:37], s[0:1]
	v_lshl_or_b32 v72, v141, 3, v0
	v_add_f32_e32 v0, v10, v11
	v_fmac_f32_e32 v10, 0x3b800000, v2
	v_add_f32_e32 v2, v16, v17
	v_pk_mul_f32 v[30:31], v[32:33], s[0:1]
	v_cvt_pk_f16_f32 v32, v0, v2
	v_accvgpr_read_b32 v35, a22
	v_cvt_f32_f16_e32 v11, v32
	v_sub_f32_e32 v6, v18, v6
	v_cvt_pk_f16_f32 v9, v4, v6
	v_accvgpr_read_b32 v4, a5
	v_pk_mul_f32 v[18:19], v[34:35], s[0:1]
	v_accvgpr_read_b32 v6, a6
	v_accvgpr_read_b32 v12, a7
	v_fmac_f32_e32 v16, 0x3b800000, v4
	v_add_f32_e32 v4, v18, v19
	v_fmac_f32_e32 v18, 0x3b800000, v6
	v_add_f32_e32 v6, v30, v31
	v_fmac_f32_e32 v30, 0x3b800000, v12
	v_cvt_pk_f16_f32 v33, v4, v6
	v_sub_f32_e32 v0, v0, v11
	v_cvt_f32_f16_sdwa v11, v32 dst_sel:DWORD dst_unused:UNUSED_PAD src0_sel:WORD_1
	v_cvt_f32_f16_e32 v12, v33
	v_cvt_f32_f16_sdwa v14, v33 dst_sel:DWORD dst_unused:UNUSED_PAD src0_sel:WORD_1
	v_cvt_pk_f16_f32 v34, v10, v16
	v_sub_f32_e32 v2, v2, v11
	v_sub_f32_e32 v4, v4, v12
	v_sub_f32_e32 v6, v6, v14
	v_cvt_f32_f16_e32 v11, v34
	v_cvt_pk_f16_f32 v36, v0, v2
	v_cvt_pk_f16_f32 v37, v4, v6
	v_cvt_pk_f16_f32 v35, v18, v30
	v_cvt_f32_f16_sdwa v2, v34 dst_sel:DWORD dst_unused:UNUSED_PAD src0_sel:WORD_1
	v_cvt_f32_f16_e32 v4, v35
	v_cvt_f32_f16_sdwa v6, v35 dst_sel:DWORD dst_unused:UNUSED_PAD src0_sel:WORD_1
	v_mad_u32_u24 v31, v76, s4, v72
	v_add_u32_e32 v38, v41, v72
	v_accvgpr_read_b32 v13, a27
	v_accvgpr_read_b32 v15, a26
	v_accvgpr_read_b32 v25, a25
	v_accvgpr_read_b32 v27, a24
	v_sub_f32_e32 v0, v10, v11
	v_sub_f32_e32 v2, v16, v2
	v_sub_f32_e32 v4, v18, v4
	v_sub_f32_e32 v6, v30, v6
	v_cvt_pk_f16_f32 v10, v0, v2
	v_cvt_pk_f16_f32 v11, v4, v6
	ds_write2_b64 v31, v[20:21], v[32:33] offset1:2
	ds_write2_b64 v38, v[22:23], v[36:37] offset1:2
	v_add_u32_e32 v23, 0x2000, v38
	v_mov_b32_e32 v14, v150
	v_mov_b32_e32 v12, v151
	ds_write2_b64 v23, v[8:9], v[10:11] offset0:64 offset1:66
	v_pk_mul_f32 v[8:9], v[26:27], s[0:1]
	v_accvgpr_read_b32 v2, a8
	v_pk_mul_f32 v[10:11], v[24:25], s[0:1]
	v_accvgpr_read_b32 v4, a9
	v_pk_mul_f32 v[14:15], v[14:15], s[0:1]
	v_accvgpr_read_b32 v6, a10
	v_pk_mul_f32 v[12:13], v[12:13], s[0:1]
	v_add_f32_e32 v0, v8, v9
	v_fmac_f32_e32 v8, 0x3b800000, v2
	v_add_f32_e32 v2, v10, v11
	v_fmac_f32_e32 v10, 0x3b800000, v4
	v_add_f32_e32 v4, v14, v15
	v_fmac_f32_e32 v14, 0x3b800000, v6
	v_add_f32_e32 v6, v12, v13
	v_accvgpr_read_b32 v9, a11
	v_cvt_pk_f16_f32 v17, v4, v6
	v_fmac_f32_e32 v12, 0x3b800000, v9
	v_cvt_f32_f16_sdwa v15, v17 dst_sel:DWORD dst_unused:UNUSED_PAD src0_sel:WORD_1
	v_cvt_pk_f16_f32 v16, v0, v2
	v_cvt_f32_f16_e32 v13, v17
	v_cvt_f32_f16_e32 v9, v16
	v_cvt_f32_f16_sdwa v11, v16 dst_sel:DWORD dst_unused:UNUSED_PAD src0_sel:WORD_1
	v_sub_f32_e32 v6, v6, v15
	v_sub_f32_e32 v4, v4, v13
	v_sub_f32_e32 v0, v0, v9
	v_cvt_pk_f16_f32 v19, v4, v6
	v_cvt_pk_f16_f32 v21, v14, v12
	v_sub_f32_e32 v2, v2, v11
	v_cvt_f32_f16_sdwa v6, v21 dst_sel:DWORD dst_unused:UNUSED_PAD src0_sel:WORD_1
	v_cvt_pk_f16_f32 v18, v0, v2
	v_cvt_pk_f16_f32 v20, v8, v10
	v_cvt_f32_f16_e32 v4, v21
	v_cvt_f32_f16_e32 v0, v20
	v_cvt_f32_f16_sdwa v2, v20 dst_sel:DWORD dst_unused:UNUSED_PAD src0_sel:WORD_1
	v_sub_f32_e32 v6, v12, v6
	v_accvgpr_read_b32 v7, a28
	v_sub_f32_e32 v0, v8, v0
	v_sub_f32_e32 v4, v14, v4
	v_cvt_pk_f16_f32 v9, v4, v6
	v_mov_b32_e32 v6, v144
	v_accvgpr_read_b32 v5, a29
	v_sub_f32_e32 v2, v10, v2
	v_cvt_pk_f16_f32 v8, v0, v2
	v_pk_mul_f32 v[6:7], v[6:7], s[0:1]
	v_accvgpr_read_b32 v0, a12
	v_mov_b32_e32 v4, v145
	v_accvgpr_read_b32 v3, a30
	v_add_f32_e32 v7, v6, v7
	v_fmac_f32_e32 v6, 0x3b800000, v0
	v_pk_mul_f32 v[4:5], v[4:5], s[0:1]
	v_accvgpr_read_b32 v0, a13
	v_mov_b32_e32 v2, v146
	v_add_f32_e32 v5, v4, v5
	v_fmac_f32_e32 v4, 0x3b800000, v0
	v_pk_mul_f32 v[2:3], v[2:3], s[0:1]
	v_accvgpr_read_b32 v0, a14
	v_accvgpr_read_b32 v1, a31
	v_add_f32_e32 v3, v2, v3
	v_fmac_f32_e32 v2, 0x3b800000, v0
	v_mov_b32_e32 v0, v147
	v_pk_mul_f32 v[0:1], v[0:1], s[0:1]
	v_accvgpr_read_b32 v10, a15
	v_add_f32_e32 v1, v0, v1
	v_cvt_pk_f16_f32 v11, v3, v1
	v_fmac_f32_e32 v0, 0x3b800000, v10
	v_cvt_f32_f16_sdwa v15, v11 dst_sel:DWORD dst_unused:UNUSED_PAD src0_sel:WORD_1
	v_cvt_pk_f16_f32 v10, v7, v5
	v_cvt_f32_f16_e32 v14, v11
	v_cvt_f32_f16_e32 v12, v10
	v_cvt_f32_f16_sdwa v13, v10 dst_sel:DWORD dst_unused:UNUSED_PAD src0_sel:WORD_1
	v_sub_f32_e32 v1, v1, v15
	v_sub_f32_e32 v3, v3, v14
	v_sub_f32_e32 v7, v7, v12
	v_sub_f32_e32 v5, v5, v13
	v_cvt_pk_f16_f32 v13, v3, v1
	v_cvt_pk_f16_f32 v14, v6, v4
	v_cvt_pk_f16_f32 v12, v7, v5
	v_cvt_pk_f16_f32 v15, v2, v0
	v_add_u32_e32 v22, 0x2000, v31
	v_cvt_f32_f16_e32 v1, v14
	v_cvt_f32_f16_sdwa v3, v14 dst_sel:DWORD dst_unused:UNUSED_PAD src0_sel:WORD_1
	v_cvt_f32_f16_e32 v5, v15
	v_cvt_f32_f16_sdwa v7, v15 dst_sel:DWORD dst_unused:UNUSED_PAD src0_sel:WORD_1
	v_sub_f32_e32 v1, v6, v1
	v_sub_f32_e32 v3, v4, v3
	v_sub_f32_e32 v2, v2, v5
	v_sub_f32_e32 v4, v0, v7
	v_cvt_pk_f16_f32 v0, v1, v3
	v_cvt_pk_f16_f32 v1, v2, v4
	ds_write2_b64 v22, v[28:29], v[34:35] offset0:64 offset1:66
	ds_write2_b64 v31, v[16:17], v[10:11] offset0:4 offset1:6
	ds_write2_b64 v38, v[18:19], v[12:13] offset0:4 offset1:6
	ds_write2_b64 v22, v[20:21], v[14:15] offset0:68 offset1:70
	ds_write2_b64 v23, v[8:9], v[0:1] offset0:68 offset1:70
	s_waitcnt lgkmcnt(0)
	s_barrier
	ds_read_b128 v[0:3], v74
	ds_read_b128 v[8:11], v74 offset:32
	ds_read_b128 v[12:15], v74 offset:8704
	ds_read_b128 v[16:19], v74 offset:8736
	v_cvt_pk_f16_f32 v4, v50, v51
	v_cvt_pk_f16_f32 v5, v52, v53
	v_cvt_pk_f16_f32 v6, v54, v55
	v_cvt_pk_f16_f32 v7, v56, v57
	v_mul_f32_e32 v28, 0x43800000, v124
	s_waitcnt lgkmcnt(3)
	v_mfma_f32_32x32x16_f16 a[0:15], v[4:7], v[0:3], 0
	v_fma_mix_f32 v20, v140, s3, -v4 op_sel_hi:[0,0,1]
	v_fma_mix_f32 v21, v136, s3, -v4 op_sel:[0,0,1] op_sel_hi:[0,0,1]
	v_fma_mix_f32 v22, v137, s3, -v5 op_sel_hi:[0,0,1]
	v_fma_mix_f32 v23, v138, s3, -v5 op_sel:[0,0,1] op_sel_hi:[0,0,1]
	v_fma_mix_f32 v24, v139, s3, -v6 op_sel_hi:[0,0,1]
	v_fma_mix_f32 v25, v133, s3, -v6 op_sel:[0,0,1] op_sel_hi:[0,0,1]
	v_fma_mix_f32 v26, v134, s3, -v7 op_sel_hi:[0,0,1]
	s_waitcnt lgkmcnt(1)
	v_mfma_f32_32x32x16_f16 a[16:31], v[4:7], v[12:15], 0
	v_fma_mix_f32 v27, v135, s3, -v7 op_sel:[0,0,1] op_sel_hi:[0,0,1]
	v_cvt_pk_f16_f32 v20, v20, v21
	v_cvt_pk_f16_f32 v21, v22, v23
	v_cvt_pk_f16_f32 v22, v24, v25
	v_cvt_pk_f16_f32 v23, v26, v27
	v_mul_f32_e32 v24, 0x43800000, v120
	v_mul_f32_e32 v25, 0x43800000, v121
	v_mfma_f32_32x32x16_f16 a[0:15], v[20:23], v[0:3], a[0:15]
	v_mul_f32_e32 v26, 0x43800000, v122
	v_mul_f32_e32 v27, 0x43800000, v123
	s_mov_b64 s[0:1], 0x2000
	v_mfma_f32_32x32x16_f16 a[16:31], v[20:23], v[12:15], a[16:31]
	ds_read_b128 v[0:3], v40
	ds_read_b128 v[12:15], v40 offset:32
	ds_read_b128 v[20:23], v40 offset:8736
	s_waitcnt lgkmcnt(2)
	v_mfma_f32_32x32x16_f16 a[0:15], v[4:7], v[0:3], a[0:15]
	ds_read_b128 v[0:3], v40 offset:8704
	s_waitcnt lgkmcnt(0)
	v_mfma_f32_32x32x16_f16 a[16:31], v[4:7], v[0:3], a[16:31]
	v_mul_f32_e32 v2, 0x43800000, v117
	v_mul_f32_e32 v3, 0x43800000, v118
	v_mul_f32_e32 v4, 0x43800000, v119
	v_cvt_pk_f16_f32 v0, v24, v25
	v_cvt_pk_f16_f32 v1, v26, v27
	v_cvt_pk_f16_f32 v2, v28, v2
	v_cvt_pk_f16_f32 v3, v3, v4
	v_mul_f32_e32 v28, 0x43800000, v116
	v_mfma_f32_32x32x16_f16 a[0:15], v[0:3], v[8:11], a[0:15]
	v_fma_mix_f32 v4, v120, s3, -v0 op_sel_hi:[0,0,1]
	v_fma_mix_f32 v5, v121, s3, -v0 op_sel:[0,0,1] op_sel_hi:[0,0,1]
	v_fma_mix_f32 v6, v122, s3, -v1 op_sel_hi:[0,0,1]
	v_fma_mix_f32 v7, v123, s3, -v1 op_sel:[0,0,1] op_sel_hi:[0,0,1]
	v_fma_mix_f32 v24, v124, s3, -v2 op_sel_hi:[0,0,1]
	v_fma_mix_f32 v25, v117, s3, -v2 op_sel:[0,0,1] op_sel_hi:[0,0,1]
	v_fma_mix_f32 v26, v118, s3, -v3 op_sel_hi:[0,0,1]
	v_mfma_f32_32x32x16_f16 a[16:31], v[0:3], v[16:19], a[16:31]
	v_fma_mix_f32 v27, v119, s3, -v3 op_sel:[0,0,1] op_sel_hi:[0,0,1]
	v_cvt_pk_f16_f32 v4, v4, v5
	v_cvt_pk_f16_f32 v5, v6, v7
	v_cvt_pk_f16_f32 v6, v24, v25
	v_cvt_pk_f16_f32 v7, v26, v27
	s_nop 0
	v_mfma_f32_32x32x16_f16 a[0:15], v[4:7], v[8:11], a[0:15]
	v_mul_f32_e32 v8, 0x43800000, v131
	v_mul_f32_e32 v9, 0x43800000, v125
	v_mul_f32_e32 v10, 0x43800000, v126
	v_mul_f32_e32 v11, 0x43800000, v127
	v_mfma_f32_32x32x16_f16 a[16:31], v[4:7], v[16:19], a[16:31]
	v_mul_f32_e32 v4, 0x43800000, v132
	v_mul_f32_e32 v5, 0x43800000, v128
	v_mul_f32_e32 v6, 0x43800000, v129
	v_mul_f32_e32 v7, 0x43800000, v130
	v_cvt_pk_f16_f32 v4, v4, v5
	v_cvt_pk_f16_f32 v5, v6, v7
	v_cvt_pk_f16_f32 v6, v8, v9
	v_mfma_f32_32x32x16_f16 a[0:15], v[0:3], v[12:15], a[0:15]
	ds_read_b128 v[12:15], v74 offset:8768
	ds_read_b128 v[16:19], v74 offset:8800
	v_cvt_pk_f16_f32 v7, v10, v11
	ds_read_b128 v[8:11], v74 offset:96
	v_fma_mix_f32 v24, v131, s3, -v6 op_sel_hi:[0,0,1]
	v_fma_mix_f32 v25, v125, s3, -v6 op_sel:[0,0,1] op_sel_hi:[0,0,1]
	v_fma_mix_f32 v26, v126, s3, -v7 op_sel_hi:[0,0,1]
	v_mfma_f32_32x32x16_f16 a[16:31], v[0:3], v[20:23], a[16:31]
	ds_read_b128 v[0:3], v74 offset:64
	v_fma_mix_f32 v20, v132, s3, -v4 op_sel_hi:[0,0,1]
	v_fma_mix_f32 v21, v128, s3, -v4 op_sel:[0,0,1] op_sel_hi:[0,0,1]
	v_fma_mix_f32 v22, v129, s3, -v5 op_sel_hi:[0,0,1]
	v_fma_mix_f32 v23, v130, s3, -v5 op_sel:[0,0,1] op_sel_hi:[0,0,1]
	v_fma_mix_f32 v27, v127, s3, -v7 op_sel:[0,0,1] op_sel_hi:[0,0,1]
	v_cvt_pk_f16_f32 v20, v20, v21
	s_waitcnt lgkmcnt(0)
	v_mfma_f32_32x32x16_f16 a[0:15], v[4:7], v[0:3], a[0:15]
	v_cvt_pk_f16_f32 v21, v22, v23
	v_cvt_pk_f16_f32 v22, v24, v25
	v_cvt_pk_f16_f32 v23, v26, v27
	v_mul_f32_e32 v24, 0x43800000, v112
	v_mul_f32_e32 v25, 0x43800000, v113
	v_mul_f32_e32 v26, 0x43800000, v114
	v_mul_f32_e32 v27, 0x43800000, v115
	v_mfma_f32_32x32x16_f16 a[16:31], v[4:7], v[12:15], a[16:31]
	v_mfma_f32_32x32x16_f16 a[0:15], v[20:23], v[0:3], a[0:15]
	v_mfma_f32_32x32x16_f16 a[16:31], v[20:23], v[12:15], a[16:31]
	ds_read_b128 v[0:3], v40 offset:64
	ds_read_b128 v[12:15], v40 offset:96
	ds_read_b128 v[20:23], v40 offset:8800
	s_waitcnt lgkmcnt(2)
	v_mfma_f32_32x32x16_f16 a[0:15], v[4:7], v[0:3], a[0:15]
	ds_read_b128 v[0:3], v40 offset:8768
	s_waitcnt lgkmcnt(0)
	v_mfma_f32_32x32x16_f16 a[16:31], v[4:7], v[0:3], a[16:31]
	v_mul_f32_e32 v2, 0x43800000, v109
	v_mul_f32_e32 v3, 0x43800000, v110
	v_mul_f32_e32 v4, 0x43800000, v111
	v_cvt_pk_f16_f32 v0, v24, v25
	v_cvt_pk_f16_f32 v1, v26, v27
	v_cvt_pk_f16_f32 v2, v28, v2
	v_cvt_pk_f16_f32 v3, v3, v4
	v_mul_f32_e32 v28, 0x43800000, v95
	v_mfma_f32_32x32x16_f16 a[0:15], v[0:3], v[8:11], a[0:15]
	v_fma_mix_f32 v4, v112, s3, -v0 op_sel_hi:[0,0,1]
	v_fma_mix_f32 v5, v113, s3, -v0 op_sel:[0,0,1] op_sel_hi:[0,0,1]
	v_fma_mix_f32 v6, v114, s3, -v1 op_sel_hi:[0,0,1]
	v_fma_mix_f32 v7, v115, s3, -v1 op_sel:[0,0,1] op_sel_hi:[0,0,1]
	v_fma_mix_f32 v24, v116, s3, -v2 op_sel_hi:[0,0,1]
	v_fma_mix_f32 v25, v109, s3, -v2 op_sel:[0,0,1] op_sel_hi:[0,0,1]
	v_fma_mix_f32 v26, v110, s3, -v3 op_sel_hi:[0,0,1]
	v_mfma_f32_32x32x16_f16 a[16:31], v[0:3], v[16:19], a[16:31]
	v_fma_mix_f32 v27, v111, s3, -v3 op_sel:[0,0,1] op_sel_hi:[0,0,1]
	v_cvt_pk_f16_f32 v4, v4, v5
	v_cvt_pk_f16_f32 v5, v6, v7
	v_cvt_pk_f16_f32 v6, v24, v25
	v_cvt_pk_f16_f32 v7, v26, v27
	s_nop 0
	v_mfma_f32_32x32x16_f16 a[0:15], v[4:7], v[8:11], a[0:15]
	v_mul_f32_e32 v8, 0x43800000, v107
	v_mul_f32_e32 v9, 0x43800000, v101
	v_mul_f32_e32 v10, 0x43800000, v102
	v_mul_f32_e32 v11, 0x43800000, v103
	v_mfma_f32_32x32x16_f16 a[16:31], v[4:7], v[16:19], a[16:31]
	v_mul_f32_e32 v4, 0x43800000, v108
	v_mul_f32_e32 v5, 0x43800000, v104
	v_mul_f32_e32 v6, 0x43800000, v105
	v_mul_f32_e32 v7, 0x43800000, v106
	v_cvt_pk_f16_f32 v4, v4, v5
	v_cvt_pk_f16_f32 v5, v6, v7
	v_cvt_pk_f16_f32 v6, v8, v9
	v_mfma_f32_32x32x16_f16 a[0:15], v[0:3], v[12:15], a[0:15]
	ds_read_b128 v[12:15], v74 offset:8832
	ds_read_b128 v[16:19], v74 offset:8864
	v_cvt_pk_f16_f32 v7, v10, v11
	ds_read_b128 v[8:11], v74 offset:160
	v_fma_mix_f32 v24, v107, s3, -v6 op_sel_hi:[0,0,1]
	v_fma_mix_f32 v25, v101, s3, -v6 op_sel:[0,0,1] op_sel_hi:[0,0,1]
	v_fma_mix_f32 v26, v102, s3, -v7 op_sel_hi:[0,0,1]
	v_mfma_f32_32x32x16_f16 a[16:31], v[0:3], v[20:23], a[16:31]
	ds_read_b128 v[0:3], v74 offset:128
	v_fma_mix_f32 v20, v108, s3, -v4 op_sel_hi:[0,0,1]
	v_fma_mix_f32 v21, v104, s3, -v4 op_sel:[0,0,1] op_sel_hi:[0,0,1]
	v_fma_mix_f32 v22, v105, s3, -v5 op_sel_hi:[0,0,1]
	v_fma_mix_f32 v23, v106, s3, -v5 op_sel:[0,0,1] op_sel_hi:[0,0,1]
	v_fma_mix_f32 v27, v103, s3, -v7 op_sel:[0,0,1] op_sel_hi:[0,0,1]
	v_cvt_pk_f16_f32 v20, v20, v21
	s_waitcnt lgkmcnt(0)
	v_mfma_f32_32x32x16_f16 a[0:15], v[4:7], v[0:3], a[0:15]
	v_cvt_pk_f16_f32 v21, v22, v23
	v_cvt_pk_f16_f32 v22, v24, v25
	v_cvt_pk_f16_f32 v23, v26, v27
	v_mul_f32_e32 v24, 0x43800000, v91
	v_mul_f32_e32 v25, 0x43800000, v92
	v_mul_f32_e32 v26, 0x43800000, v93
	v_mul_f32_e32 v27, 0x43800000, v94
	v_mfma_f32_32x32x16_f16 a[16:31], v[4:7], v[12:15], a[16:31]
	v_mfma_f32_32x32x16_f16 a[0:15], v[20:23], v[0:3], a[0:15]
	v_mfma_f32_32x32x16_f16 a[16:31], v[20:23], v[12:15], a[16:31]
	ds_read_b128 v[0:3], v40 offset:128
	ds_read_b128 v[12:15], v40 offset:160
	ds_read_b128 v[20:23], v40 offset:8864
	s_waitcnt lgkmcnt(2)
	v_mfma_f32_32x32x16_f16 a[0:15], v[4:7], v[0:3], a[0:15]
	ds_read_b128 v[0:3], v40 offset:8832
	s_waitcnt lgkmcnt(0)
	v_mfma_f32_32x32x16_f16 a[16:31], v[4:7], v[0:3], a[16:31]
	v_mul_f32_e32 v2, 0x43800000, v88
	v_mul_f32_e32 v3, 0x43800000, v89
	v_mul_f32_e32 v4, 0x43800000, v90
	v_cvt_pk_f16_f32 v0, v24, v25
	v_cvt_pk_f16_f32 v1, v26, v27
	v_cvt_pk_f16_f32 v2, v28, v2
	v_cvt_pk_f16_f32 v3, v3, v4
	v_mul_f32_e32 v28, 0x43800000, v84
	v_mfma_f32_32x32x16_f16 a[0:15], v[0:3], v[8:11], a[0:15]
	v_fma_mix_f32 v4, v91, s3, -v0 op_sel_hi:[0,0,1]
	v_fma_mix_f32 v5, v92, s3, -v0 op_sel:[0,0,1] op_sel_hi:[0,0,1]
	v_fma_mix_f32 v6, v93, s3, -v1 op_sel_hi:[0,0,1]
	v_fma_mix_f32 v7, v94, s3, -v1 op_sel:[0,0,1] op_sel_hi:[0,0,1]
	v_fma_mix_f32 v24, v95, s3, -v2 op_sel_hi:[0,0,1]
	v_fma_mix_f32 v25, v88, s3, -v2 op_sel:[0,0,1] op_sel_hi:[0,0,1]
	v_fma_mix_f32 v26, v89, s3, -v3 op_sel_hi:[0,0,1]
	v_mfma_f32_32x32x16_f16 a[16:31], v[0:3], v[16:19], a[16:31]
	v_fma_mix_f32 v27, v90, s3, -v3 op_sel:[0,0,1] op_sel_hi:[0,0,1]
	v_cvt_pk_f16_f32 v4, v4, v5
	v_cvt_pk_f16_f32 v5, v6, v7
	v_cvt_pk_f16_f32 v6, v24, v25
	v_cvt_pk_f16_f32 v7, v26, v27
	s_nop 0
	v_mfma_f32_32x32x16_f16 a[0:15], v[4:7], v[8:11], a[0:15]
	v_mul_f32_e32 v8, 0x43800000, v99
	v_mul_f32_e32 v9, 0x43800000, v85
	v_mul_f32_e32 v10, 0x43800000, v86
	v_mul_f32_e32 v11, 0x43800000, v87
	v_mfma_f32_32x32x16_f16 a[16:31], v[4:7], v[16:19], a[16:31]
	v_mul_f32_e32 v4, 0x43800000, v100
	v_mul_f32_e32 v5, 0x43800000, v96
	v_mul_f32_e32 v6, 0x43800000, v97
	v_mul_f32_e32 v7, 0x43800000, v98
	v_cvt_pk_f16_f32 v4, v4, v5
	v_cvt_pk_f16_f32 v5, v6, v7
	v_cvt_pk_f16_f32 v6, v8, v9
	v_mfma_f32_32x32x16_f16 a[0:15], v[0:3], v[12:15], a[0:15]
	ds_read_b128 v[12:15], v74 offset:8896
	ds_read_b128 v[16:19], v74 offset:8928
	v_cvt_pk_f16_f32 v7, v10, v11
	ds_read_b128 v[8:11], v74 offset:224
	v_fma_mix_f32 v24, v99, s3, -v6 op_sel_hi:[0,0,1]
	v_fma_mix_f32 v25, v85, s3, -v6 op_sel:[0,0,1] op_sel_hi:[0,0,1]
	v_fma_mix_f32 v26, v86, s3, -v7 op_sel_hi:[0,0,1]
	v_mfma_f32_32x32x16_f16 a[16:31], v[0:3], v[20:23], a[16:31]
	ds_read_b128 v[0:3], v74 offset:192
	v_fma_mix_f32 v20, v100, s3, -v4 op_sel_hi:[0,0,1]
	v_fma_mix_f32 v21, v96, s3, -v4 op_sel:[0,0,1] op_sel_hi:[0,0,1]
	v_fma_mix_f32 v22, v97, s3, -v5 op_sel_hi:[0,0,1]
	v_fma_mix_f32 v23, v98, s3, -v5 op_sel:[0,0,1] op_sel_hi:[0,0,1]
	v_fma_mix_f32 v27, v87, s3, -v7 op_sel:[0,0,1] op_sel_hi:[0,0,1]
	v_cvt_pk_f16_f32 v20, v20, v21
	s_waitcnt lgkmcnt(0)
	v_mfma_f32_32x32x16_f16 a[0:15], v[4:7], v[0:3], a[0:15]
	v_cvt_pk_f16_f32 v21, v22, v23
	v_cvt_pk_f16_f32 v22, v24, v25
	v_cvt_pk_f16_f32 v23, v26, v27
	v_mul_f32_e32 v24, 0x43800000, v80
	v_mul_f32_e32 v25, 0x43800000, v81
	v_mul_f32_e32 v26, 0x43800000, v82
	v_mul_f32_e32 v27, 0x43800000, v83
	v_mfma_f32_32x32x16_f16 a[16:31], v[4:7], v[12:15], a[16:31]
	v_or_b32_e32 v74, s2, v76
	v_mfma_f32_32x32x16_f16 a[0:15], v[20:23], v[0:3], a[0:15]
	v_mfma_f32_32x32x16_f16 a[16:31], v[20:23], v[12:15], a[16:31]
	ds_read_b128 v[0:3], v40 offset:192
	ds_read_b128 v[12:15], v40 offset:224
	ds_read_b128 v[20:23], v40 offset:8928
	s_waitcnt lgkmcnt(2)
	v_mfma_f32_32x32x16_f16 a[0:15], v[4:7], v[0:3], a[0:15]
	ds_read_b128 v[0:3], v40 offset:8896
	s_waitcnt lgkmcnt(0)
	v_mfma_f32_32x32x16_f16 a[16:31], v[4:7], v[0:3], a[16:31]
	v_mul_f32_e32 v2, 0x43800000, v77
	v_mul_f32_e32 v3, 0x43800000, v78
	v_mul_f32_e32 v4, 0x43800000, v79
	v_cvt_pk_f16_f32 v0, v24, v25
	v_cvt_pk_f16_f32 v1, v26, v27
	v_cvt_pk_f16_f32 v2, v28, v2
	v_cvt_pk_f16_f32 v3, v3, v4
	s_nop 0
	v_mfma_f32_32x32x16_f16 a[0:15], v[0:3], v[8:11], a[0:15]
	v_fma_mix_f32 v4, v80, s3, -v0 op_sel_hi:[0,0,1]
	v_fma_mix_f32 v5, v81, s3, -v0 op_sel:[0,0,1] op_sel_hi:[0,0,1]
	v_fma_mix_f32 v6, v82, s3, -v1 op_sel_hi:[0,0,1]
	v_fma_mix_f32 v7, v83, s3, -v1 op_sel:[0,0,1] op_sel_hi:[0,0,1]
	v_fma_mix_f32 v24, v84, s3, -v2 op_sel_hi:[0,0,1]
	v_fma_mix_f32 v25, v77, s3, -v2 op_sel:[0,0,1] op_sel_hi:[0,0,1]
	v_fma_mix_f32 v26, v78, s3, -v3 op_sel_hi:[0,0,1]
	v_mfma_f32_32x32x16_f16 a[16:31], v[0:3], v[16:19], a[16:31]
	v_fma_mix_f32 v27, v79, s3, -v3 op_sel:[0,0,1] op_sel_hi:[0,0,1]
	v_cvt_pk_f16_f32 v4, v4, v5
	v_cvt_pk_f16_f32 v5, v6, v7
	v_cvt_pk_f16_f32 v6, v24, v25
	v_cvt_pk_f16_f32 v7, v26, v27
	s_nop 0
	v_mfma_f32_32x32x16_f16 a[0:15], v[4:7], v[8:11], a[0:15]
	v_mfma_f32_32x32x16_f16 a[16:31], v[4:7], v[16:19], a[16:31]
	v_mfma_f32_32x32x16_f16 a[0:15], v[0:3], v[12:15], a[0:15]
	v_mfma_f32_32x32x16_f16 a[16:31], v[0:3], v[20:23], a[16:31]
	s_nop 15
	s_barrier
	v_and_b32_e32 v10, 31, v187
	v_bfe_u32 v11, v187, 5, 1
	v_lshrrev_b32_e32 v12, 6, v187
	v_and_b32_e32 v13, 63, v187
	v_lshrrev_b32_e32 v14, 4, v13
	v_and_b32_e32 v15, 15, v13
	v_and_b32_e32 v16, 15, v10
	v_lshlrev_b32_e32 v16, 4, v16
	v_lshlrev_b32_e32 v17, 8, v10
	v_lshl_add_u32 v17, v11, 3, v17
	v_lshlrev_b32_e32 v18, 6, v12
	v_xor_b32_e32 v18, v18, v16
	v_xor_b32_e32 v19, v15, v14
	v_lshlrev_b32_e32 v19, 4, v19
	v_lshl_add_u32 v20, v12, 4, v14
	v_lshlrev_b32_e32 v21, 8, v20
	v_add_u32_e32 v22, s2, v20
	v_mov_b32_e32 v23, 0
	v_lshlrev_b64 v[22:23], 8, v[22:23]
	v_lshl_add_u64 v[22:23], v[22:23], 0, s[12:13]
	v_lshlrev_b32_e32 v24, 4, v15
	v_mov_b32_e32 v25, 0
	v_lshl_add_u64 v[22:23], v[22:23], 0, v[24:25]
	v_accvgpr_read_b32 v44, a0
	v_accvgpr_read_b32 v45, a1
	v_accvgpr_read_b32 v46, a2
	v_accvgpr_read_b32 v47, a3
	v_mul_f32_e32 v44, 0x39b8aa3b, v44
	v_mul_f32_e32 v45, 0x39b8aa3b, v45
	v_mul_f32_e32 v46, 0x39b8aa3b, v46
	v_mul_f32_e32 v47, 0x39b8aa3b, v47
	v_cvt_pk_f16_f32 v44, v44, v45
	v_cvt_pk_f16_f32 v45, v46, v47
	v_xor_b32_e32 v48, 0x0, v18
	v_add_u32_e32 v48, v48, v17
	ds_write_b64 v48, v[44:45] offset:0
	v_accvgpr_read_b32 v52, a4
	v_accvgpr_read_b32 v53, a5
	v_accvgpr_read_b32 v54, a6
	v_accvgpr_read_b32 v55, a7
	v_mul_f32_e32 v52, 0x39b8aa3b, v52
	v_mul_f32_e32 v53, 0x39b8aa3b, v53
	v_mul_f32_e32 v54, 0x39b8aa3b, v54
	v_mul_f32_e32 v55, 0x39b8aa3b, v55
	v_cvt_pk_f16_f32 v52, v52, v53
	v_cvt_pk_f16_f32 v53, v54, v55
	v_xor_b32_e32 v56, 0x10, v18
	v_add_u32_e32 v56, v56, v17
	ds_write_b64 v56, v[52:53] offset:0
	v_accvgpr_read_b32 v60, a8
	v_accvgpr_read_b32 v61, a9
	v_accvgpr_read_b32 v62, a10
	v_accvgpr_read_b32 v63, a11
	v_mul_f32_e32 v60, 0x39b8aa3b, v60
	v_mul_f32_e32 v61, 0x39b8aa3b, v61
	v_mul_f32_e32 v62, 0x39b8aa3b, v62
	v_mul_f32_e32 v63, 0x39b8aa3b, v63
	v_cvt_pk_f16_f32 v60, v60, v61
	v_cvt_pk_f16_f32 v61, v62, v63
	v_xor_b32_e32 v64, 0x20, v18
	v_add_u32_e32 v64, v64, v17
	ds_write_b64 v64, v[60:61] offset:0
	v_accvgpr_read_b32 v68, a12
	v_accvgpr_read_b32 v69, a13
	v_accvgpr_read_b32 v70, a14
	v_accvgpr_read_b32 v71, a15
	v_mul_f32_e32 v68, 0x39b8aa3b, v68
	v_mul_f32_e32 v69, 0x39b8aa3b, v69
	v_mul_f32_e32 v70, 0x39b8aa3b, v70
	v_mul_f32_e32 v71, 0x39b8aa3b, v71
	v_cvt_pk_f16_f32 v68, v68, v69
	v_cvt_pk_f16_f32 v69, v70, v71
	v_xor_b32_e32 v72, 0x30, v18
	v_add_u32_e32 v72, v72, v17
	ds_write_b64 v72, v[68:69] offset:0
	v_accvgpr_read_b32 v76, a16
	v_accvgpr_read_b32 v77, a17
	v_accvgpr_read_b32 v78, a18
	v_accvgpr_read_b32 v79, a19
	v_mul_f32_e32 v76, 0x39b8aa3b, v76
	v_mul_f32_e32 v77, 0x39b8aa3b, v77
	v_mul_f32_e32 v78, 0x39b8aa3b, v78
	v_mul_f32_e32 v79, 0x39b8aa3b, v79
	v_cvt_pk_f16_f32 v76, v76, v77
	v_cvt_pk_f16_f32 v77, v78, v79
	v_xor_b32_e32 v80, 0x0, v18
	v_add_u32_e32 v80, v80, v17
	ds_write_b64 v80, v[76:77] offset:8192
	v_accvgpr_read_b32 v84, a20
	v_accvgpr_read_b32 v85, a21
	v_accvgpr_read_b32 v86, a22
	v_accvgpr_read_b32 v87, a23
	v_mul_f32_e32 v84, 0x39b8aa3b, v84
	v_mul_f32_e32 v85, 0x39b8aa3b, v85
	v_mul_f32_e32 v86, 0x39b8aa3b, v86
	v_mul_f32_e32 v87, 0x39b8aa3b, v87
	v_cvt_pk_f16_f32 v84, v84, v85
	v_cvt_pk_f16_f32 v85, v86, v87
	v_xor_b32_e32 v88, 0x10, v18
	v_add_u32_e32 v88, v88, v17
	ds_write_b64 v88, v[84:85] offset:8192
	v_accvgpr_read_b32 v92, a24
	v_accvgpr_read_b32 v93, a25
	v_accvgpr_read_b32 v94, a26
	v_accvgpr_read_b32 v95, a27
	v_mul_f32_e32 v92, 0x39b8aa3b, v92
	v_mul_f32_e32 v93, 0x39b8aa3b, v93
	v_mul_f32_e32 v94, 0x39b8aa3b, v94
	v_mul_f32_e32 v95, 0x39b8aa3b, v95
	v_cvt_pk_f16_f32 v92, v92, v93
	v_cvt_pk_f16_f32 v93, v94, v95
	v_xor_b32_e32 v96, 0x20, v18
	v_add_u32_e32 v96, v96, v17
	ds_write_b64 v96, v[92:93] offset:8192
	v_accvgpr_read_b32 v100, a28
	v_accvgpr_read_b32 v101, a29
	v_accvgpr_read_b32 v102, a30
	v_accvgpr_read_b32 v103, a31
	v_mul_f32_e32 v100, 0x39b8aa3b, v100
	v_mul_f32_e32 v101, 0x39b8aa3b, v101
	v_mul_f32_e32 v102, 0x39b8aa3b, v102
	v_mul_f32_e32 v103, 0x39b8aa3b, v103
	v_cvt_pk_f16_f32 v100, v100, v101
	v_cvt_pk_f16_f32 v101, v102, v103
	v_xor_b32_e32 v104, 0x30, v18
	v_add_u32_e32 v104, v104, v17
	ds_write_b64 v104, v[100:101] offset:8192
	s_waitcnt lgkmcnt(0)
	s_barrier
	v_xor_b32_e32 v27, 0x0, v19
	v_add_u32_e32 v27, v27, v21
	ds_read_b128 v[28:31], v27 offset:0
	v_xor_b32_e32 v27, 0x40, v19
	v_add_u32_e32 v27, v27, v21
	ds_read_b128 v[32:35], v27 offset:1024
	v_xor_b32_e32 v27, 0x80, v19
	v_add_u32_e32 v27, v27, v21
	ds_read_b128 v[36:39], v27 offset:2048
	v_xor_b32_e32 v27, 0xc0, v19
	v_add_u32_e32 v27, v27, v21
	ds_read_b128 v[40:43], v27 offset:3072
	s_waitcnt lgkmcnt(3)
	global_store_dwordx4 v[22:23], v[28:31], off offset:0 sc1
	s_waitcnt lgkmcnt(2)
	global_store_dwordx4 v[22:23], v[32:35], off offset:1024 sc1
	s_waitcnt lgkmcnt(1)
	global_store_dwordx4 v[22:23], v[36:39], off offset:2048 sc1
	s_waitcnt lgkmcnt(0)
	global_store_dwordx4 v[22:23], v[40:43], off offset:3072 sc1
	s_endpgm

_Z19combine_proj_kernelPKDF16_PK15HIP_vector_typeIfLj2EES0_PKfPf:
	s_load_dwordx8 s[4:11], s[0:1], 0x0
	s_load_dwordx2 s[12:13], s[0:1], 0x20
	v_and_b32_e32 v1, 15, v0
	v_lshrrev_b32_e32 v2, 4, v0
	s_lshl_b32 s3, s2, 9
	s_lshl_b32 s14, s2, 14
	s_lshl_b32 s15, s2, 15
	v_lshl_add_u32 v3, v2, 3, s3
	v_lshlrev_b32_e32 v4, 8, v2
	v_lshl_add_u32 v4, v1, 4, v4
	v_add_u32_e32 v4, s14, v4
	v_add_u32_e32 v5, 0x1000, v4
	v_add_u32_e32 v6, 0x2000, v4
	v_add_u32_e32 v7, 0x3000, v4
	v_lshrrev_b32_e32 v8, 6, v0
	v_and_b32_e32 v9, 63, v0
	v_and_b32_e32 v10, 31, v0
	v_bfe_u32 v11, v0, 5, 1
	v_and_b32_e32 v18, 1, v8
	v_lshrrev_b32_e32 v19, 1, v8
	v_lshlrev_b32_e32 v12, 14, v19
	v_lshl_add_u32 v12, v10, 8, v12
	v_lshl_add_u32 v12, v11, 4, v12
	v_add_u32_e32 v13, 0x2000, v12
	v_lshlrev_b32_e32 v14, 8, v19
	v_lshl_add_u32 v14, v10, 2, v14
	s_waitcnt lgkmcnt(0)
	s_add_u32 s16, s6, 0x20000
	s_addc_u32 s17, s7, 0
	s_add_u32 s18, s6, 0x40000
	s_addc_u32 s19, s7, 0
	s_add_u32 s20, s6, 0x60000
	s_addc_u32 s21, s7, 0
	s_add_u32 s22, s4, 0x400000
	s_addc_u32 s23, s5, 0
	s_add_u32 s24, s4, 0x800000
	s_addc_u32 s25, s5, 0
	s_add_u32 s26, s4, 0xc00000
	s_addc_u32 s27, s5, 0
	global_load_dwordx2 v[20:21], v3, s[6:7] offset:0
	global_load_dwordx2 v[22:23], v3, s[16:17] offset:0
	global_load_dwordx2 v[24:25], v3, s[18:19] offset:0
	global_load_dwordx2 v[26:27], v3, s[20:21] offset:0
	global_load_dwordx2 v[28:29], v3, s[6:7] offset:128
	global_load_dwordx2 v[30:31], v3, s[16:17] offset:128
	global_load_dwordx2 v[32:33], v3, s[18:19] offset:128
	global_load_dwordx2 v[34:35], v3, s[20:21] offset:128
	global_load_dwordx2 v[36:37], v3, s[6:7] offset:256
	global_load_dwordx2 v[38:39], v3, s[16:17] offset:256
	global_load_dwordx2 v[40:41], v3, s[18:19] offset:256
	global_load_dwordx2 v[42:43], v3, s[20:21] offset:256
	global_load_dwordx2 v[44:45], v3, s[6:7] offset:384
	global_load_dwordx2 v[46:47], v3, s[16:17] offset:384
	global_load_dwordx2 v[48:49], v3, s[18:19] offset:384
	global_load_dwordx2 v[50:51], v3, s[20:21] offset:384
	global_load_dwordx4 v[52:55], v4, s[4:5]
	global_load_dwordx4 v[56:59], v4, s[22:23]
	global_load_dwordx4 v[60:63], v4, s[24:25]
	global_load_dwordx4 v[64:67], v4, s[26:27]
	global_load_dwordx4 v[68:71], v5, s[4:5]
	global_load_dwordx4 v[72:75], v5, s[22:23]
	global_load_dwordx4 v[76:79], v5, s[24:25]
	global_load_dwordx4 v[80:83], v5, s[26:27]
	global_load_dwordx4 v[84:87], v6, s[4:5]
	global_load_dwordx4 v[88:91], v6, s[22:23]
	global_load_dwordx4 v[92:95], v6, s[24:25]
	global_load_dwordx4 v[96:99], v6, s[26:27]
	global_load_dwordx4 v[100:103], v7, s[4:5]
	global_load_dwordx4 v[104:107], v7, s[22:23]
	global_load_dwordx4 v[108:111], v7, s[24:25]
	global_load_dwordx4 v[112:115], v7, s[26:27]
	global_load_dwordx4 v[116:119], v12, s[8:9] offset:0
	global_load_dwordx4 v[120:123], v12, s[8:9] offset:32
	global_load_dwordx4 v[124:127], v12, s[8:9] offset:64
	global_load_dwordx4 v[128:131], v12, s[8:9] offset:96
	global_load_dwordx4 v[132:135], v12, s[8:9] offset:128
	global_load_dwordx4 v[136:139], v12, s[8:9] offset:160
	global_load_dwordx4 v[140:143], v12, s[8:9] offset:192
	global_load_dwordx4 v[144:147], v12, s[8:9] offset:224
	global_load_dwordx4 v[148:151], v13, s[8:9] offset:0
	global_load_dwordx4 v[152:155], v13, s[8:9] offset:32
	global_load_dwordx4 v[156:159], v13, s[8:9] offset:64
	global_load_dwordx4 v[160:163], v13, s[8:9] offset:96
	global_load_dwordx4 v[164:167], v13, s[8:9] offset:128
	global_load_dwordx4 v[168:171], v13, s[8:9] offset:160
	global_load_dwordx4 v[172:175], v13, s[8:9] offset:192
	global_load_dwordx4 v[176:179], v13, s[8:9] offset:224
	global_load_dword v180, v14, s[10:11]
	global_load_dword v181, v14, s[10:11] offset:128
	v_mul_u32_u24_e32 v15, 0x110, v2
	v_lshl_add_u32 v15, v1, 4, v15
	v_lshl_add_u32 v16, v18, 5, v10
	v_mul_u32_u24_e32 v16, 0x110, v16
	v_lshl_add_u32 v16, v11, 4, v16
	v_lshlrev_b32_e32 v17, 14, v18
	v_lshl_add_u32 v17, v11, 11, v17
	v_add3_u32 v17, v17, v14, s15
	s_mov_b32 s28, s12
	s_and_b32 s29, s13, 0xffff
	s_mov_b32 s30, 0x800000
	s_mov_b32 s31, 0x20000
	s_movk_i32 s33, 0x1000
	s_movk_i32 s34, 0x2000
	s_movk_i32 s35, 0x3000
	s_waitcnt vmcnt(30)
	v_max3_f32 v182, v20, v22, v24
	v_max_f32_e32 v182, v182, v26
	v_sub_f32_e32 v183, v20, v182
	v_sub_f32_e32 v184, v22, v182
	v_sub_f32_e32 v185, v24, v182
	v_sub_f32_e32 v186, v26, v182
	v_exp_f32_e32 v183, v183
	v_exp_f32_e32 v184, v184
	v_exp_f32_e32 v185, v185
	v_exp_f32_e32 v186, v186
	s_nop 0
	v_mul_f32_e32 v183, v183, v21
	v_mul_f32_e32 v184, v184, v23
	v_mul_f32_e32 v185, v185, v25
	v_mul_f32_e32 v186, v186, v27
	v_add_f32_e32 v187, v183, v184
	v_add_f32_e32 v187, v187, v185
	v_add_f32_e32 v187, v187, v186
	v_rcp_f32_e32 v187, v187
	s_nop 0
	v_mul_f32_e32 v188, v183, v187
	v_mul_f32_e32 v189, v184, v187
	v_mul_f32_e32 v190, v185, v187
	v_mul_f32_e32 v191, v186, v187
	v_fma_mix_f32 v192, v188, v52, 0 op_sel_hi:[0,1,0]
	v_fma_mix_f32 v193, v188, v52, 0 op_sel:[0,1,0] op_sel_hi:[0,1,0]
	v_fma_mix_f32 v194, v188, v53, 0 op_sel_hi:[0,1,0]
	v_fma_mix_f32 v195, v188, v53, 0 op_sel:[0,1,0] op_sel_hi:[0,1,0]
	v_fma_mix_f32 v196, v188, v54, 0 op_sel_hi:[0,1,0]
	v_fma_mix_f32 v197, v188, v54, 0 op_sel:[0,1,0] op_sel_hi:[0,1,0]
	v_fma_mix_f32 v198, v188, v55, 0 op_sel_hi:[0,1,0]
	v_fma_mix_f32 v199, v188, v55, 0 op_sel:[0,1,0] op_sel_hi:[0,1,0]
	v_fma_mix_f32 v192, v189, v56, v192 op_sel_hi:[0,1,0]
	v_fma_mix_f32 v193, v189, v56, v193 op_sel:[0,1,0] op_sel_hi:[0,1,0]
	v_fma_mix_f32 v194, v189, v57, v194 op_sel_hi:[0,1,0]
	v_fma_mix_f32 v195, v189, v57, v195 op_sel:[0,1,0] op_sel_hi:[0,1,0]
	v_fma_mix_f32 v196, v189, v58, v196 op_sel_hi:[0,1,0]
	v_fma_mix_f32 v197, v189, v58, v197 op_sel:[0,1,0] op_sel_hi:[0,1,0]
	v_fma_mix_f32 v198, v189, v59, v198 op_sel_hi:[0,1,0]
	v_fma_mix_f32 v199, v189, v59, v199 op_sel:[0,1,0] op_sel_hi:[0,1,0]
	v_fma_mix_f32 v192, v190, v60, v192 op_sel_hi:[0,1,0]
	v_fma_mix_f32 v193, v190, v60, v193 op_sel:[0,1,0] op_sel_hi:[0,1,0]
	v_fma_mix_f32 v194, v190, v61, v194 op_sel_hi:[0,1,0]
	v_fma_mix_f32 v195, v190, v61, v195 op_sel:[0,1,0] op_sel_hi:[0,1,0]
	v_fma_mix_f32 v196, v190, v62, v196 op_sel_hi:[0,1,0]
	v_fma_mix_f32 v197, v190, v62, v197 op_sel:[0,1,0] op_sel_hi:[0,1,0]
	v_fma_mix_f32 v198, v190, v63, v198 op_sel_hi:[0,1,0]
	v_fma_mix_f32 v199, v190, v63, v199 op_sel:[0,1,0] op_sel_hi:[0,1,0]
	v_fma_mix_f32 v192, v191, v64, v192 op_sel_hi:[0,1,0]
	v_fma_mix_f32 v193, v191, v64, v193 op_sel:[0,1,0] op_sel_hi:[0,1,0]
	v_fma_mix_f32 v194, v191, v65, v194 op_sel_hi:[0,1,0]
	v_fma_mix_f32 v195, v191, v65, v195 op_sel:[0,1,0] op_sel_hi:[0,1,0]
	v_fma_mix_f32 v196, v191, v66, v196 op_sel_hi:[0,1,0]
	v_fma_mix_f32 v197, v191, v66, v197 op_sel:[0,1,0] op_sel_hi:[0,1,0]
	v_fma_mix_f32 v198, v191, v67, v198 op_sel_hi:[0,1,0]
	v_fma_mix_f32 v199, v191, v67, v199 op_sel:[0,1,0] op_sel_hi:[0,1,0]
	v_cvt_pk_f16_f32 v200, v192, v193
	v_cvt_pk_f16_f32 v201, v194, v195
	v_cvt_pk_f16_f32 v202, v196, v197
	v_cvt_pk_f16_f32 v203, v198, v199
	ds_write_b128 v15, v[200:203] offset:0
	s_waitcnt vmcnt(26)
	v_max3_f32 v182, v28, v30, v32
	v_max_f32_e32 v182, v182, v34
	v_sub_f32_e32 v183, v28, v182
	v_sub_f32_e32 v184, v30, v182
	v_sub_f32_e32 v185, v32, v182
	v_sub_f32_e32 v186, v34, v182
	v_exp_f32_e32 v183, v183
	v_exp_f32_e32 v184, v184
	v_exp_f32_e32 v185, v185
	v_exp_f32_e32 v186, v186
	s_nop 0
	v_mul_f32_e32 v183, v183, v29
	v_mul_f32_e32 v184, v184, v31
	v_mul_f32_e32 v185, v185, v33
	v_mul_f32_e32 v186, v186, v35
	v_add_f32_e32 v187, v183, v184
	v_add_f32_e32 v187, v187, v185
	v_add_f32_e32 v187, v187, v186
	v_rcp_f32_e32 v187, v187
	s_nop 0
	v_mul_f32_e32 v188, v183, v187
	v_mul_f32_e32 v189, v184, v187
	v_mul_f32_e32 v190, v185, v187
	v_mul_f32_e32 v191, v186, v187
	v_fma_mix_f32 v192, v188, v68, 0 op_sel_hi:[0,1,0]
	v_fma_mix_f32 v193, v188, v68, 0 op_sel:[0,1,0] op_sel_hi:[0,1,0]
	v_fma_mix_f32 v194, v188, v69, 0 op_sel_hi:[0,1,0]
	v_fma_mix_f32 v195, v188, v69, 0 op_sel:[0,1,0] op_sel_hi:[0,1,0]
	v_fma_mix_f32 v196, v188, v70, 0 op_sel_hi:[0,1,0]
	v_fma_mix_f32 v197, v188, v70, 0 op_sel:[0,1,0] op_sel_hi:[0,1,0]
	v_fma_mix_f32 v198, v188, v71, 0 op_sel_hi:[0,1,0]
	v_fma_mix_f32 v199, v188, v71, 0 op_sel:[0,1,0] op_sel_hi:[0,1,0]
	v_fma_mix_f32 v192, v189, v72, v192 op_sel_hi:[0,1,0]
	v_fma_mix_f32 v193, v189, v72, v193 op_sel:[0,1,0] op_sel_hi:[0,1,0]
	v_fma_mix_f32 v194, v189, v73, v194 op_sel_hi:[0,1,0]
	v_fma_mix_f32 v195, v189, v73, v195 op_sel:[0,1,0] op_sel_hi:[0,1,0]
	v_fma_mix_f32 v196, v189, v74, v196 op_sel_hi:[0,1,0]
	v_fma_mix_f32 v197, v189, v74, v197 op_sel:[0,1,0] op_sel_hi:[0,1,0]
	v_fma_mix_f32 v198, v189, v75, v198 op_sel_hi:[0,1,0]
	v_fma_mix_f32 v199, v189, v75, v199 op_sel:[0,1,0] op_sel_hi:[0,1,0]
	v_fma_mix_f32 v192, v190, v76, v192 op_sel_hi:[0,1,0]
	v_fma_mix_f32 v193, v190, v76, v193 op_sel:[0,1,0] op_sel_hi:[0,1,0]
	v_fma_mix_f32 v194, v190, v77, v194 op_sel_hi:[0,1,0]
	v_fma_mix_f32 v195, v190, v77, v195 op_sel:[0,1,0] op_sel_hi:[0,1,0]
	v_fma_mix_f32 v196, v190, v78, v196 op_sel_hi:[0,1,0]
	v_fma_mix_f32 v197, v190, v78, v197 op_sel:[0,1,0] op_sel_hi:[0,1,0]
	v_fma_mix_f32 v198, v190, v79, v198 op_sel_hi:[0,1,0]
	v_fma_mix_f32 v199, v190, v79, v199 op_sel:[0,1,0] op_sel_hi:[0,1,0]
	v_fma_mix_f32 v192, v191, v80, v192 op_sel_hi:[0,1,0]
	v_fma_mix_f32 v193, v191, v80, v193 op_sel:[0,1,0] op_sel_hi:[0,1,0]
	v_fma_mix_f32 v194, v191, v81, v194 op_sel_hi:[0,1,0]
	v_fma_mix_f32 v195, v191, v81, v195 op_sel:[0,1,0] op_sel_hi:[0,1,0]
	v_fma_mix_f32 v196, v191, v82, v196 op_sel_hi:[0,1,0]
	v_fma_mix_f32 v197, v191, v82, v197 op_sel:[0,1,0] op_sel_hi:[0,1,0]
	v_fma_mix_f32 v198, v191, v83, v198 op_sel_hi:[0,1,0]
	v_fma_mix_f32 v199, v191, v83, v199 op_sel:[0,1,0] op_sel_hi:[0,1,0]
	v_cvt_pk_f16_f32 v200, v192, v193
	v_cvt_pk_f16_f32 v201, v194, v195
	v_cvt_pk_f16_f32 v202, v196, v197
	v_cvt_pk_f16_f32 v203, v198, v199
	ds_write_b128 v15, v[200:203] offset:4352
	s_waitcnt vmcnt(22)
	v_max3_f32 v182, v36, v38, v40
	v_max_f32_e32 v182, v182, v42
	v_sub_f32_e32 v183, v36, v182
	v_sub_f32_e32 v184, v38, v182
	v_sub_f32_e32 v185, v40, v182
	v_sub_f32_e32 v186, v42, v182
	v_exp_f32_e32 v183, v183
	v_exp_f32_e32 v184, v184
	v_exp_f32_e32 v185, v185
	v_exp_f32_e32 v186, v186
	s_nop 0
	v_mul_f32_e32 v183, v183, v37
	v_mul_f32_e32 v184, v184, v39
	v_mul_f32_e32 v185, v185, v41
	v_mul_f32_e32 v186, v186, v43
	v_add_f32_e32 v187, v183, v184
	v_add_f32_e32 v187, v187, v185
	v_add_f32_e32 v187, v187, v186
	v_rcp_f32_e32 v187, v187
	s_nop 0
	v_mul_f32_e32 v188, v183, v187
	v_mul_f32_e32 v189, v184, v187
	v_mul_f32_e32 v190, v185, v187
	v_mul_f32_e32 v191, v186, v187
	v_fma_mix_f32 v192, v188, v84, 0 op_sel_hi:[0,1,0]
	v_fma_mix_f32 v193, v188, v84, 0 op_sel:[0,1,0] op_sel_hi:[0,1,0]
	v_fma_mix_f32 v194, v188, v85, 0 op_sel_hi:[0,1,0]
	v_fma_mix_f32 v195, v188, v85, 0 op_sel:[0,1,0] op_sel_hi:[0,1,0]
	v_fma_mix_f32 v196, v188, v86, 0 op_sel_hi:[0,1,0]
	v_fma_mix_f32 v197, v188, v86, 0 op_sel:[0,1,0] op_sel_hi:[0,1,0]
	v_fma_mix_f32 v198, v188, v87, 0 op_sel_hi:[0,1,0]
	v_fma_mix_f32 v199, v188, v87, 0 op_sel:[0,1,0] op_sel_hi:[0,1,0]
	v_fma_mix_f32 v192, v189, v88, v192 op_sel_hi:[0,1,0]
	v_fma_mix_f32 v193, v189, v88, v193 op_sel:[0,1,0] op_sel_hi:[0,1,0]
	v_fma_mix_f32 v194, v189, v89, v194 op_sel_hi:[0,1,0]
	v_fma_mix_f32 v195, v189, v89, v195 op_sel:[0,1,0] op_sel_hi:[0,1,0]
	v_fma_mix_f32 v196, v189, v90, v196 op_sel_hi:[0,1,0]
	v_fma_mix_f32 v197, v189, v90, v197 op_sel:[0,1,0] op_sel_hi:[0,1,0]
	v_fma_mix_f32 v198, v189, v91, v198 op_sel_hi:[0,1,0]
	v_fma_mix_f32 v199, v189, v91, v199 op_sel:[0,1,0] op_sel_hi:[0,1,0]
	v_fma_mix_f32 v192, v190, v92, v192 op_sel_hi:[0,1,0]
	v_fma_mix_f32 v193, v190, v92, v193 op_sel:[0,1,0] op_sel_hi:[0,1,0]
	v_fma_mix_f32 v194, v190, v93, v194 op_sel_hi:[0,1,0]
	v_fma_mix_f32 v195, v190, v93, v195 op_sel:[0,1,0] op_sel_hi:[0,1,0]
	v_fma_mix_f32 v196, v190, v94, v196 op_sel_hi:[0,1,0]
	v_fma_mix_f32 v197, v190, v94, v197 op_sel:[0,1,0] op_sel_hi:[0,1,0]
	v_fma_mix_f32 v198, v190, v95, v198 op_sel_hi:[0,1,0]
	v_fma_mix_f32 v199, v190, v95, v199 op_sel:[0,1,0] op_sel_hi:[0,1,0]
	v_fma_mix_f32 v192, v191, v96, v192 op_sel_hi:[0,1,0]
	v_fma_mix_f32 v193, v191, v96, v193 op_sel:[0,1,0] op_sel_hi:[0,1,0]
	v_fma_mix_f32 v194, v191, v97, v194 op_sel_hi:[0,1,0]
	v_fma_mix_f32 v195, v191, v97, v195 op_sel:[0,1,0] op_sel_hi:[0,1,0]
	v_fma_mix_f32 v196, v191, v98, v196 op_sel_hi:[0,1,0]
	v_fma_mix_f32 v197, v191, v98, v197 op_sel:[0,1,0] op_sel_hi:[0,1,0]
	v_fma_mix_f32 v198, v191, v99, v198 op_sel_hi:[0,1,0]
	v_fma_mix_f32 v199, v191, v99, v199 op_sel:[0,1,0] op_sel_hi:[0,1,0]
	v_cvt_pk_f16_f32 v200, v192, v193
	v_cvt_pk_f16_f32 v201, v194, v195
	v_cvt_pk_f16_f32 v202, v196, v197
	v_cvt_pk_f16_f32 v203, v198, v199
	ds_write_b128 v15, v[200:203] offset:8704
	s_waitcnt vmcnt(18)
	v_max3_f32 v182, v44, v46, v48
	v_max_f32_e32 v182, v182, v50
	v_sub_f32_e32 v183, v44, v182
	v_sub_f32_e32 v184, v46, v182
	v_sub_f32_e32 v185, v48, v182
	v_sub_f32_e32 v186, v50, v182
	v_exp_f32_e32 v183, v183
	v_exp_f32_e32 v184, v184
	v_exp_f32_e32 v185, v185
	v_exp_f32_e32 v186, v186
	s_nop 0
	v_mul_f32_e32 v183, v183, v45
	v_mul_f32_e32 v184, v184, v47
	v_mul_f32_e32 v185, v185, v49
	v_mul_f32_e32 v186, v186, v51
	v_add_f32_e32 v187, v183, v184
	v_add_f32_e32 v187, v187, v185
	v_add_f32_e32 v187, v187, v186
	v_rcp_f32_e32 v187, v187
	s_nop 0
	v_mul_f32_e32 v188, v183, v187
	v_mul_f32_e32 v189, v184, v187
	v_mul_f32_e32 v190, v185, v187
	v_mul_f32_e32 v191, v186, v187
	v_fma_mix_f32 v192, v188, v100, 0 op_sel_hi:[0,1,0]
	v_fma_mix_f32 v193, v188, v100, 0 op_sel:[0,1,0] op_sel_hi:[0,1,0]
	v_fma_mix_f32 v194, v188, v101, 0 op_sel_hi:[0,1,0]
	v_fma_mix_f32 v195, v188, v101, 0 op_sel:[0,1,0] op_sel_hi:[0,1,0]
	v_fma_mix_f32 v196, v188, v102, 0 op_sel_hi:[0,1,0]
	v_fma_mix_f32 v197, v188, v102, 0 op_sel:[0,1,0] op_sel_hi:[0,1,0]
	v_fma_mix_f32 v198, v188, v103, 0 op_sel_hi:[0,1,0]
	v_fma_mix_f32 v199, v188, v103, 0 op_sel:[0,1,0] op_sel_hi:[0,1,0]
	v_fma_mix_f32 v192, v189, v104, v192 op_sel_hi:[0,1,0]
	v_fma_mix_f32 v193, v189, v104, v193 op_sel:[0,1,0] op_sel_hi:[0,1,0]
	v_fma_mix_f32 v194, v189, v105, v194 op_sel_hi:[0,1,0]
	v_fma_mix_f32 v195, v189, v105, v195 op_sel:[0,1,0] op_sel_hi:[0,1,0]
	v_fma_mix_f32 v196, v189, v106, v196 op_sel_hi:[0,1,0]
	v_fma_mix_f32 v197, v189, v106, v197 op_sel:[0,1,0] op_sel_hi:[0,1,0]
	v_fma_mix_f32 v198, v189, v107, v198 op_sel_hi:[0,1,0]
	v_fma_mix_f32 v199, v189, v107, v199 op_sel:[0,1,0] op_sel_hi:[0,1,0]
	v_fma_mix_f32 v192, v190, v108, v192 op_sel_hi:[0,1,0]
	v_fma_mix_f32 v193, v190, v108, v193 op_sel:[0,1,0] op_sel_hi:[0,1,0]
	v_fma_mix_f32 v194, v190, v109, v194 op_sel_hi:[0,1,0]
	v_fma_mix_f32 v195, v190, v109, v195 op_sel:[0,1,0] op_sel_hi:[0,1,0]
	v_fma_mix_f32 v196, v190, v110, v196 op_sel_hi:[0,1,0]
	v_fma_mix_f32 v197, v190, v110, v197 op_sel:[0,1,0] op_sel_hi:[0,1,0]
	v_fma_mix_f32 v198, v190, v111, v198 op_sel_hi:[0,1,0]
	v_fma_mix_f32 v199, v190, v111, v199 op_sel:[0,1,0] op_sel_hi:[0,1,0]
	v_fma_mix_f32 v192, v191, v112, v192 op_sel_hi:[0,1,0]
	v_fma_mix_f32 v193, v191, v112, v193 op_sel:[0,1,0] op_sel_hi:[0,1,0]
	v_fma_mix_f32 v194, v191, v113, v194 op_sel_hi:[0,1,0]
	v_fma_mix_f32 v195, v191, v113, v195 op_sel:[0,1,0] op_sel_hi:[0,1,0]
	v_fma_mix_f32 v196, v191, v114, v196 op_sel_hi:[0,1,0]
	v_fma_mix_f32 v197, v191, v114, v197 op_sel:[0,1,0] op_sel_hi:[0,1,0]
	v_fma_mix_f32 v198, v191, v115, v198 op_sel_hi:[0,1,0]
	v_fma_mix_f32 v199, v191, v115, v199 op_sel:[0,1,0] op_sel_hi:[0,1,0]
	v_cvt_pk_f16_f32 v200, v192, v193
	v_cvt_pk_f16_f32 v201, v194, v195
	v_cvt_pk_f16_f32 v202, v196, v197
	v_cvt_pk_f16_f32 v203, v198, v199
	ds_write_b128 v15, v[200:203] offset:13056
	s_waitcnt lgkmcnt(0)
	s_barrier
	ds_read_b128 v[52:55], v16 offset:0
	ds_read_b128 v[56:59], v16 offset:32
	ds_read_b128 v[60:63], v16 offset:64
	ds_read_b128 v[64:67], v16 offset:96
	ds_read_b128 v[68:71], v16 offset:128
	ds_read_b128 v[72:75], v16 offset:160
	ds_read_b128 v[76:79], v16 offset:192
	ds_read_b128 v[80:83], v16 offset:224
	s_waitcnt vmcnt(0)
	s_waitcnt lgkmcnt(7)
	v_mfma_f32_32x32x16_f16 v[84:99], v[52:55], v[116:119], 0
	v_mfma_f32_32x32x16_f16 v[100:115], v[52:55], v[148:151], 0
	s_waitcnt lgkmcnt(6)
	v_mfma_f32_32x32x16_f16 v[84:99], v[56:59], v[120:123], v[84:99]
	v_mfma_f32_32x32x16_f16 v[100:115], v[56:59], v[152:155], v[100:115]
	s_waitcnt lgkmcnt(5)
	v_mfma_f32_32x32x16_f16 v[84:99], v[60:63], v[124:127], v[84:99]
	v_mfma_f32_32x32x16_f16 v[100:115], v[60:63], v[156:159], v[100:115]
	s_waitcnt lgkmcnt(4)
	v_mfma_f32_32x32x16_f16 v[84:99], v[64:67], v[128:131], v[84:99]
	v_mfma_f32_32x32x16_f16 v[100:115], v[64:67], v[160:163], v[100:115]
	s_waitcnt lgkmcnt(3)
	v_mfma_f32_32x32x16_f16 v[84:99], v[68:71], v[132:135], v[84:99]
	v_mfma_f32_32x32x16_f16 v[100:115], v[68:71], v[164:167], v[100:115]
	s_waitcnt lgkmcnt(2)
	v_mfma_f32_32x32x16_f16 v[84:99], v[72:75], v[136:139], v[84:99]
	v_mfma_f32_32x32x16_f16 v[100:115], v[72:75], v[168:171], v[100:115]
	s_waitcnt lgkmcnt(1)
	v_mfma_f32_32x32x16_f16 v[84:99], v[76:79], v[140:143], v[84:99]
	v_mfma_f32_32x32x16_f16 v[100:115], v[76:79], v[172:175], v[100:115]
	s_waitcnt lgkmcnt(0)
	v_mfma_f32_32x32x16_f16 v[84:99], v[80:83], v[144:147], v[84:99]
	v_mfma_f32_32x32x16_f16 v[100:115], v[80:83], v[176:179], v[100:115]
	s_nop 15
	v_lshlrev_b32_e32 v182, 13, v8
	v_add_u32_e32 v182, 0x4400, v182
	v_lshl_add_u32 v183, v11, 10, v182
	v_lshl_add_u32 v183, v10, 2, v183
	v_lshrrev_b32_e32 v184, 4, v9
	v_and_b32_e32 v185, 15, v9
	v_lshl_add_u32 v186, v184, 8, v182
	v_lshl_add_u32 v186, v185, 4, v186
	v_lshlrev_b32_e32 v187, 14, v18
	v_lshl_add_u32 v187, v184, 9, v187
	v_lshl_add_u32 v187, v19, 8, v187
	v_lshl_add_u32 v187, v185, 4, v187
	v_add_u32_e32 v187, s15, v187
	s_movk_i32 s36, 0x0
	s_movk_i32 s37, 0x800
	s_movk_i32 s38, 0x1000
	s_movk_i32 s39, 0x1800
	s_movk_i32 s40, 0x2000
	s_movk_i32 s41, 0x2800
	s_movk_i32 s42, 0x3000
	s_movk_i32 s43, 0x3800
	v_add_f32_e32 v84, v84, v180
	v_max_f32_e32 v84, 0, v84
	ds_write_b32 v183, v84 offset:0
	v_add_f32_e32 v85, v85, v180
	v_max_f32_e32 v85, 0, v85
	ds_write_b32 v183, v85 offset:256
	v_add_f32_e32 v86, v86, v180
	v_max_f32_e32 v86, 0, v86
	ds_write_b32 v183, v86 offset:512
	v_add_f32_e32 v87, v87, v180
	v_max_f32_e32 v87, 0, v87
	ds_write_b32 v183, v87 offset:768
	v_add_f32_e32 v88, v88, v180
	v_max_f32_e32 v88, 0, v88
	ds_write_b32 v183, v88 offset:2048
	v_add_f32_e32 v89, v89, v180
	v_max_f32_e32 v89, 0, v89
	ds_write_b32 v183, v89 offset:2304
	v_add_f32_e32 v90, v90, v180
	v_max_f32_e32 v90, 0, v90
	ds_write_b32 v183, v90 offset:2560
	v_add_f32_e32 v91, v91, v180
	v_max_f32_e32 v91, 0, v91
	ds_write_b32 v183, v91 offset:2816
	v_add_f32_e32 v92, v92, v180
	v_max_f32_e32 v92, 0, v92
	ds_write_b32 v183, v92 offset:4096
	v_add_f32_e32 v93, v93, v180
	v_max_f32_e32 v93, 0, v93
	ds_write_b32 v183, v93 offset:4352
	v_add_f32_e32 v94, v94, v180
	v_max_f32_e32 v94, 0, v94
	ds_write_b32 v183, v94 offset:4608
	v_add_f32_e32 v95, v95, v180
	v_max_f32_e32 v95, 0, v95
	ds_write_b32 v183, v95 offset:4864
	v_add_f32_e32 v96, v96, v180
	v_max_f32_e32 v96, 0, v96
	ds_write_b32 v183, v96 offset:6144
	v_add_f32_e32 v97, v97, v180
	v_max_f32_e32 v97, 0, v97
	ds_write_b32 v183, v97 offset:6400
	v_add_f32_e32 v98, v98, v180
	v_max_f32_e32 v98, 0, v98
	ds_write_b32 v183, v98 offset:6656
	v_add_f32_e32 v99, v99, v180
	v_max_f32_e32 v99, 0, v99
	ds_write_b32 v183, v99 offset:6912
	v_add_f32_e32 v100, v100, v181
	v_max_f32_e32 v100, 0, v100
	ds_write_b32 v183, v100 offset:128
	v_add_f32_e32 v101, v101, v181
	v_max_f32_e32 v101, 0, v101
	ds_write_b32 v183, v101 offset:384
	v_add_f32_e32 v102, v102, v181
	v_max_f32_e32 v102, 0, v102
	ds_write_b32 v183, v102 offset:640
	v_add_f32_e32 v103, v103, v181
	v_max_f32_e32 v103, 0, v103
	ds_write_b32 v183, v103 offset:896
	v_add_f32_e32 v104, v104, v181
	v_max_f32_e32 v104, 0, v104
	ds_write_b32 v183, v104 offset:2176
	v_add_f32_e32 v105, v105, v181
	v_max_f32_e32 v105, 0, v105
	ds_write_b32 v183, v105 offset:2432
	v_add_f32_e32 v106, v106, v181
	v_max_f32_e32 v106, 0, v106
	ds_write_b32 v183, v106 offset:2688
	v_add_f32_e32 v107, v107, v181
	v_max_f32_e32 v107, 0, v107
	ds_write_b32 v183, v107 offset:2944
	v_add_f32_e32 v108, v108, v181
	v_max_f32_e32 v108, 0, v108
	ds_write_b32 v183, v108 offset:4224
	v_add_f32_e32 v109, v109, v181
	v_max_f32_e32 v109, 0, v109
	ds_write_b32 v183, v109 offset:4480
	v_add_f32_e32 v110, v110, v181
	v_max_f32_e32 v110, 0, v110
	ds_write_b32 v183, v110 offset:4736
	v_add_f32_e32 v111, v111, v181
	v_max_f32_e32 v111, 0, v111
	ds_write_b32 v183, v111 offset:4992
	v_add_f32_e32 v112, v112, v181
	v_max_f32_e32 v112, 0, v112
	ds_write_b32 v183, v112 offset:6272
	v_add_f32_e32 v113, v113, v181
	v_max_f32_e32 v113, 0, v113
	ds_write_b32 v183, v113 offset:6528
	v_add_f32_e32 v114, v114, v181
	v_max_f32_e32 v114, 0, v114
	ds_write_b32 v183, v114 offset:6784
	v_add_f32_e32 v115, v115, v181
	v_max_f32_e32 v115, 0, v115
	ds_write_b32 v183, v115 offset:7040
	s_waitcnt lgkmcnt(0)
	ds_read_b128 v[52:55], v186 offset:0
	ds_read_b128 v[56:59], v186 offset:1024
	ds_read_b128 v[60:63], v186 offset:2048
	ds_read_b128 v[64:67], v186 offset:3072
	ds_read_b128 v[68:71], v186 offset:4096
	ds_read_b128 v[72:75], v186 offset:5120
	ds_read_b128 v[76:79], v186 offset:6144
	ds_read_b128 v[80:83], v186 offset:7168
	s_waitcnt lgkmcnt(7)
	buffer_store_dwordx4 v[52:55], v187, s[28:31], s36 offen sc1
	s_waitcnt lgkmcnt(6)
	buffer_store_dwordx4 v[56:59], v187, s[28:31], s37 offen sc1
	s_waitcnt lgkmcnt(5)
	buffer_store_dwordx4 v[60:63], v187, s[28:31], s38 offen sc1
	s_waitcnt lgkmcnt(4)
	buffer_store_dwordx4 v[64:67], v187, s[28:31], s39 offen sc1
	s_waitcnt lgkmcnt(3)
	buffer_store_dwordx4 v[68:71], v187, s[28:31], s40 offen sc1
	s_waitcnt lgkmcnt(2)
	buffer_store_dwordx4 v[72:75], v187, s[28:31], s41 offen sc1
	s_waitcnt lgkmcnt(1)
	buffer_store_dwordx4 v[76:79], v187, s[28:31], s42 offen sc1
	s_waitcnt lgkmcnt(0)
	buffer_store_dwordx4 v[80:83], v187, s[28:31], s43 offen sc1
	s_endpgm

	.amdhsa_kernel _Z19combine_proj_kernelPKDF16_PK15HIP_vector_typeIfLj2EES0_PKfPf
		.amdhsa_group_segment_fixed_size 50176
		.amdhsa_private_segment_fixed_size 0
		.amdhsa_kernarg_size 40
		.amdhsa_user_sgpr_count 2
		.amdhsa_user_sgpr_dispatch_ptr 0
		.amdhsa_user_sgpr_queue_ptr 0
		.amdhsa_user_sgpr_kernarg_segment_ptr 1
		.amdhsa_user_sgpr_dispatch_id 0
		.amdhsa_user_sgpr_kernarg_preload_length 0
		.amdhsa_user_sgpr_kernarg_preload_offset 0
		.amdhsa_user_sgpr_private_segment_size 0
		.amdhsa_uses_dynamic_stack 0
		.amdhsa_enable_private_segment 0
		.amdhsa_system_sgpr_workgroup_id_x 1
		.amdhsa_system_sgpr_workgroup_id_y 0
		.amdhsa_system_sgpr_workgroup_id_z 0
		.amdhsa_system_sgpr_workgroup_info 0
		.amdhsa_system_vgpr_workitem_id 0
		.amdhsa_next_free_vgpr 208
		.amdhsa_next_free_sgpr 44
		.amdhsa_accum_offset 204
		.amdhsa_reserve_vcc 1
		.amdhsa_float_round_mode_32 0
		.amdhsa_float_round_mode_16_64 0
		.amdhsa_float_denorm_mode_32 3
		.amdhsa_float_denorm_mode_16_64 3
		.amdhsa_dx10_clamp 1
		.amdhsa_ieee_mode 1
		.amdhsa_fp16_overflow 0
		.amdhsa_tg_split 0
		.amdhsa_exception_fp_ieee_invalid_op 0
		.amdhsa_exception_fp_denorm_src 0
		.amdhsa_exception_fp_ieee_div_zero 0
		.amdhsa_exception_fp_ieee_overflow 0
		.amdhsa_exception_fp_ieee_underflow 0
		.amdhsa_exception_fp_ieee_inexact 0
		.amdhsa_exception_int_div_zero 0
	.end_amdhsa_kernel

amdhsa.kernels:
  - .agpr_count:     32
    .args:
      - .actual_access:  read_only
        .address_space:  global
        .offset:         0
        .size:           8
        .value_kind:     global_buffer
      - .actual_access:  read_only
        .address_space:  global
        .offset:         8
        .size:           8
        .value_kind:     global_buffer
      - .actual_access:  read_only
        .address_space:  global
        .offset:         16
        .size:           8
        .value_kind:     global_buffer
      - .actual_access:  read_only
        .address_space:  global
        .offset:         24
        .size:           8
        .value_kind:     global_buffer
      - .actual_access:  write_only
        .address_space:  global
        .offset:         32
        .size:           8
        .value_kind:     global_buffer
      - .actual_access:  write_only
        .address_space:  global
        .offset:         40
        .size:           8
        .value_kind:     global_buffer
      - .actual_access:  read_only
        .address_space:  global
        .offset:         48
        .size:           8
        .value_kind:     global_buffer
      - .actual_access:  write_only
        .address_space:  global
        .offset:         56
        .size:           8
        .value_kind:     global_buffer
    .group_segment_fixed_size: 34816
    .kernarg_segment_align: 8
    .kernarg_segment_size: 64
    .language:       OpenCL C
    .language_version:
      - 2
      - 0
    .max_flat_workgroup_size: 256
    .name:           _Z11prep_kernelPKfS0_S0_S0_PDF16_S1_S0_S1_
    .private_segment_fixed_size: 0
    .sgpr_count:     30
    .sgpr_spill_count: 0
    .symbol:         _Z11prep_kernelPKfS0_S0_S0_PDF16_S1_S0_S1_.kd
    .uniform_work_group_size: 1
    .uses_dynamic_stack: false
    .vgpr_count:     220
    .vgpr_spill_count: 0
    .wavefront_size: 64
  - .agpr_count:     0
    .args:
      - .actual_access:  read_only
        .address_space:  global
        .offset:         0
        .size:           8
        .value_kind:     global_buffer
      - .address_space:  global
        .offset:         8
        .size:           8
        .value_kind:     global_buffer
      - .actual_access:  write_only
        .address_space:  global
        .offset:         16
        .size:           8
        .value_kind:     global_buffer
      - .actual_access:  write_only
        .address_space:  global
        .offset:         24
        .size:           8
        .value_kind:     global_buffer
    .group_segment_fixed_size: 16384
    .kernarg_segment_align: 8
    .kernarg_segment_size: 32
    .language:       OpenCL C
    .language_version:
      - 2
      - 0
    .max_flat_workgroup_size: 512
    .name:           _Z11attn_kernelPKDF16_S0_PDF16_P15HIP_vector_typeIfLj2EE
    .private_segment_fixed_size: 0
    .sgpr_count:     46
    .sgpr_spill_count: 0
    .symbol:         _Z11attn_kernelPKDF16_S0_PDF16_P15HIP_vector_typeIfLj2EE.kd
    .uniform_work_group_size: 1
    .uses_dynamic_stack: false
    .vgpr_count:     244
    .vgpr_spill_count: 0
    .wavefront_size: 64
  - .agpr_count:     0
    .args:
      - .actual_access:  read_only
        .address_space:  global
        .offset:         0
        .size:           8
        .value_kind:     global_buffer
      - .actual_access:  read_only
        .address_space:  global
        .offset:         8
        .size:           8
        .value_kind:     global_buffer
      - .actual_access:  read_only
        .address_space:  global
        .offset:         16
        .size:           8
        .value_kind:     global_buffer
      - .actual_access:  read_only
        .address_space:  global
        .offset:         24
        .size:           8
        .value_kind:     global_buffer
      - .actual_access:  write_only
        .address_space:  global
        .offset:         32
        .size:           8
        .value_kind:     global_buffer
    .group_segment_fixed_size: 50176
    .kernarg_segment_align: 8
    .kernarg_segment_size: 40
    .language:       OpenCL C
    .language_version:
      - 2
      - 0
    .max_flat_workgroup_size: 256
    .name:           _Z19combine_proj_kernelPKDF16_PK15HIP_vector_typeIfLj2EES0_PKfPf
    .private_segment_fixed_size: 0
    .sgpr_count:     50
    .sgpr_spill_count: 0
    .symbol:         _Z19combine_proj_kernelPKDF16_PK15HIP_vector_typeIfLj2EES0_PKfPf.kd
    .uniform_work_group_size: 1
    .uses_dynamic_stack: false
    .vgpr_count:     220
    .vgpr_spill_count: 0
    .wavefront_size: 64
